# baseline (speedup 1.0000x reference)
.LBB7_9:
	v_lshrrev_b32_e32 v3, 6, v0
	v_mul_u32_u24_e32 v3, 0x1200, v3
	s_waitcnt vmcnt(6)
	s_nop 5
	v_accvgpr_read_b32 v23, a0
	v_accvgpr_read_b32 v22, a1
	v_lshl_or_b32 v12, v12, 2, v3
	s_movk_i32 s5, 0x240
	v_accvgpr_read_b32 v21, a2
	v_accvgpr_read_b32 v20, a3
	v_fma_f32 v23, s6, v23, v13
	v_mad_u32_u24 v12, v14, s5, v12
	v_fma_f32 v14, s6, v22, v13
	v_accvgpr_read_b32 v19, a4
	v_accvgpr_read_b32 v18, a5
	s_waitcnt lgkmcnt(0)
	s_barrier
	ds_write2_b32 v12, v23, v14 offset1:36
	v_fma_f32 v14, s6, v21, v13
	v_fma_f32 v20, s6, v20, v13
	v_and_b32_e32 v2, 63, v0
	v_accvgpr_read_b32 v17, a6
	v_accvgpr_read_b32 v16, a7
	ds_write2_b32 v12, v14, v20 offset0:72 offset1:108
	v_fma_f32 v14, s6, v19, v13
	v_fma_f32 v18, s6, v18, v13
	v_add_u32_e32 v19, 0x400, v12
	v_lshlrev_b32_e32 v0, 2, v0
	v_accvgpr_read_b32 v15, a8
	v_accvgpr_read_b32 v10, a9
	v_accvgpr_read_b32 v9, a10
	v_accvgpr_read_b32 v8, a11
	v_accvgpr_read_b32 v7, a12
	v_accvgpr_read_b32 v6, a13
	v_accvgpr_read_b32 v5, a14
	v_accvgpr_read_b32 v4, a15
	ds_write2_b32 v19, v14, v18 offset0:32 offset1:68
	v_fma_f32 v14, s6, v17, v13
	v_fma_f32 v16, s6, v16, v13
	v_and_b32_e32 v0, 28, v0
	ds_write2_b32 v19, v14, v16 offset0:104 offset1:140
	v_fma_f32 v14, s6, v15, v13
	v_fma_f32 v10, s6, v10, v13
	v_add_u32_e32 v15, 0x800, v12
	v_fma_f32 v9, s6, v9, v13
	v_fma_f32 v8, s6, v8, v13
	v_fma_f32 v7, s6, v7, v13
	v_fma_f32 v6, s6, v6, v13
	v_fma_f32 v5, s6, v5, v13
	v_fmac_f32_e32 v13, s6, v4
	v_or3_b32 v4, s2, v1, v0
	ds_write2_b32 v15, v9, v8 offset0:136 offset1:172
	v_add_u32_e32 v8, 0xc00, v12
	v_cmp_gt_i32_e32 vcc, s4, v4
	ds_write2_b32 v15, v14, v10 offset0:64 offset1:100
	ds_write2_b32 v8, v7, v6 offset0:96 offset1:132
	ds_write2_b32 v8, v5, v13 offset0:168 offset1:204
	s_and_saveexec_b64 s[4:5], vcc
	s_cbranch_execz .LBB7_11
	s_load_dwordx2 s[0:1], s[0:1], 0x40
	v_add_u32_e32 v4, s3, v11
	v_ashrrev_i32_e32 v5, 31, v4
	s_ashr_i32 s3, s2, 31
	v_lshlrev_b32_e32 v0, 2, v0
	s_waitcnt lgkmcnt(0)
	v_mul_lo_u32 v6, s0, v5
	v_mul_lo_u32 v7, s1, v4
	v_mad_u64_u32 v[4:5], s[4:5], s0, v4, 0
	v_add3_u32 v5, v5, v6, v7
	v_lshl_add_u64 v[4:5], v[4:5], 2, s[8:9]
	v_lshl_add_u64 v[4:5], s[2:3], 2, v[4:5]
	v_lshlrev_b32_e32 v6, 2, v1
	v_mov_b32_e32 v7, 0
	v_lshl_add_u64 v[4:5], v[4:5], 0, v[6:7]
	v_mov_b32_e32 v1, v7
	v_lshrrev_b32_e32 v12, 3, v2
	v_lshl_add_u64 v[8:9], v[4:5], 0, v[0:1]
	v_mul_u32_u24_e32 v1, 0x90, v12
	v_add3_u32 v13, v3, v0, v1
	ds_read_b128 v[0:3], v13
	v_mad_u64_u32 v[4:5], s[2:3], s0, v12, 0
	v_mov_b32_e32 v6, v5
	v_mad_u64_u32 v[6:7], s[2:3], s1, v12, v[6:7]
	v_mov_b32_e32 v5, v6
	v_lshl_add_u64 v[10:11], v[4:5], 2, v[8:9]
	ds_read_b128 v[4:7], v13 offset:1152
	s_waitcnt lgkmcnt(1)
	global_store_dwordx4 v[10:11], v[0:3], off
	s_nop 1
	v_or_b32_e32 v3, 8, v12
	v_mad_u64_u32 v[0:1], s[2:3], s0, v3, 0
	v_mov_b32_e32 v2, v1
	v_mad_u64_u32 v[2:3], s[2:3], s1, v3, v[2:3]
	v_mov_b32_e32 v1, v2
	v_lshl_add_u64 v[0:1], v[0:1], 2, v[8:9]
	s_waitcnt lgkmcnt(0)
	global_store_dwordx4 v[0:1], v[4:7], off
	ds_read_b128 v[0:3], v13 offset:2304
	s_nop 0
	v_or_b32_e32 v7, 16, v12
	v_mad_u64_u32 v[4:5], s[2:3], s0, v7, 0
	v_mov_b32_e32 v6, v5
	v_mad_u64_u32 v[6:7], s[2:3], s1, v7, v[6:7]
	v_mov_b32_e32 v5, v6
	v_lshl_add_u64 v[10:11], v[4:5], 2, v[8:9]
	ds_read_b128 v[4:7], v13 offset:3456
	s_waitcnt lgkmcnt(1)
	global_store_dwordx4 v[10:11], v[0:3], off
	s_nop 1
	v_or_b32_e32 v3, 24, v12
	v_mad_u64_u32 v[0:1], s[2:3], s0, v3, 0
	v_mov_b32_e32 v2, v1
	v_mad_u64_u32 v[2:3], s[0:1], s1, v3, v[2:3]
	v_mov_b32_e32 v1, v2
	v_lshl_add_u64 v[0:1], v[0:1], 2, v[8:9]
	s_waitcnt lgkmcnt(0)
	global_store_dwordx4 v[0:1], v[4:7], off

.LBB11_7:
	v_lshrrev_b32_e32 v3, 6, v0
	v_mul_u32_u24_e32 v3, 0x1200, v3
	s_waitcnt vmcnt(6)
	s_nop 5
	v_accvgpr_read_b32 v20, a2
	v_accvgpr_read_b32 v19, a3
	v_lshl_or_b32 v23, v1, 2, v3
	s_movk_i32 s2, 0x240
	v_accvgpr_read_b32 v16, a6
	v_accvgpr_read_b32 v15, a7
	v_mad_u32_u24 v12, v12, s2, v23
	v_fma_f32 v20, s6, v20, 0
	v_fma_f32 v19, s6, v19, 0
	v_accvgpr_read_b32 v9, a10
	v_accvgpr_read_b32 v8, a11
	s_waitcnt lgkmcnt(0)
	s_barrier
	ds_write2_b32 v12, v20, v19 offset0:72 offset1:108
	v_add_u32_e32 v19, 0x400, v12
	v_fma_f32 v16, s6, v16, 0
	v_fma_f32 v15, s6, v15, 0
	v_and_b32_e32 v2, 63, v0
	v_accvgpr_read_b32 v5, a14
	v_accvgpr_read_b32 v4, a15
	ds_write2_b32 v19, v16, v15 offset0:104 offset1:140
	v_add_u32_e32 v15, 0x800, v12
	v_fma_f32 v9, s6, v9, 0
	v_fma_f32 v8, s6, v8, 0
	v_lshlrev_b32_e32 v0, 2, v0
	ds_write2_b32 v15, v9, v8 offset0:136 offset1:172
	v_add_u32_e32 v8, 0xc00, v12
	v_fma_f32 v5, s6, v5, 0
	v_fma_f32 v4, s6, v4, 0
	v_and_b32_e32 v0, 28, v0
	v_accvgpr_read_b32 v22, a0
	v_accvgpr_read_b32 v21, a1
	v_accvgpr_read_b32 v18, a4
	v_accvgpr_read_b32 v17, a5
	v_accvgpr_read_b32 v14, a8
	v_accvgpr_read_b32 v13, a9
	v_accvgpr_read_b32 v7, a12
	v_accvgpr_read_b32 v6, a13
	ds_write2_b32 v8, v5, v4 offset0:168 offset1:204
	v_or3_b32 v4, v10, v0, s16
	v_mov_b32_e32 v1, 0
	v_fma_f32 v22, s6, v22, 0
	v_fma_f32 v21, s6, v21, 0
	v_fma_f32 v18, s6, v18, 0
	v_fma_f32 v17, s6, v17, 0
	v_fma_f32 v14, s6, v14, 0
	v_fma_f32 v13, s6, v13, 0
	v_fma_f32 v7, s6, v7, 0
	v_fma_f32 v6, s6, v6, 0
	v_cmp_gt_i32_e32 vcc, s4, v4
	ds_write2_b32 v12, v22, v21 offset1:36
	ds_write2_b32 v19, v18, v17 offset0:32 offset1:68
	ds_write2_b32 v15, v14, v13 offset0:64 offset1:100
	ds_write2_b32 v8, v7, v6 offset0:96 offset1:132
	s_and_saveexec_b64 s[2:3], vcc
	s_cbranch_execz .LBB11_9
	s_load_dwordx4 s[0:3], s[0:1], 0x40
	s_ashr_i32 s4, s17, 31
	v_lshlrev_b32_e32 v4, 2, v0
	v_add_u32_e32 v0, s7, v11
	v_ashrrev_i32_e32 v5, 31, v0
	s_waitcnt lgkmcnt(0)
	s_mul_hi_u32 s5, s2, s17
	s_mul_i32 s4, s2, s4
	s_mul_i32 s3, s3, s17
	s_add_i32 s4, s5, s4
	s_add_i32 s3, s4, s3
	s_mul_i32 s2, s2, s17
	s_lshl_b64 s[2:3], s[2:3], 2
	s_add_u32 s2, s8, s2
	v_mul_lo_u32 v5, s0, v5
	v_mul_lo_u32 v8, s1, v0
	v_mad_u64_u32 v[6:7], s[4:5], s0, v0, 0
	s_addc_u32 s3, s9, s3
	v_add3_u32 v7, v7, v5, v8
	v_lshl_add_u64 v[6:7], v[6:7], 2, s[2:3]
	s_ashr_i32 s17, s16, 31
	v_lshl_add_u64 v[6:7], s[16:17], 2, v[6:7]
	v_lshlrev_b32_e32 v0, 2, v10
	v_lshrrev_b32_e32 v12, 3, v2
	v_lshl_add_u64 v[6:7], v[6:7], 0, v[0:1]
	v_mul_u32_u24_e32 v0, 0x90, v12
	v_mov_b32_e32 v5, v1
	v_add3_u32 v13, v3, v4, v0
	v_lshl_add_u64 v[8:9], v[6:7], 0, v[4:5]
	ds_read_b128 v[0:3], v13
	v_mad_u64_u32 v[4:5], s[2:3], s0, v12, 0
	v_mov_b32_e32 v6, v5
	v_mad_u64_u32 v[6:7], s[2:3], s1, v12, v[6:7]
	v_mov_b32_e32 v5, v6
	v_lshl_add_u64 v[10:11], v[4:5], 2, v[8:9]
	ds_read_b128 v[4:7], v13 offset:1152
	s_waitcnt lgkmcnt(1)
	global_store_dwordx4 v[10:11], v[0:3], off
	s_nop 1
	v_or_b32_e32 v3, 8, v12
	v_mad_u64_u32 v[0:1], s[2:3], s0, v3, 0
	v_mov_b32_e32 v2, v1
	v_mad_u64_u32 v[2:3], s[2:3], s1, v3, v[2:3]
	v_mov_b32_e32 v1, v2
	v_lshl_add_u64 v[0:1], v[0:1], 2, v[8:9]
	s_waitcnt lgkmcnt(0)
	global_store_dwordx4 v[0:1], v[4:7], off
	ds_read_b128 v[0:3], v13 offset:2304
	s_nop 0
	v_or_b32_e32 v7, 16, v12
	v_mad_u64_u32 v[4:5], s[2:3], s0, v7, 0
	v_mov_b32_e32 v6, v5
	v_mad_u64_u32 v[6:7], s[2:3], s1, v7, v[6:7]
	v_mov_b32_e32 v5, v6
	v_lshl_add_u64 v[10:11], v[4:5], 2, v[8:9]
	ds_read_b128 v[4:7], v13 offset:3456
	s_waitcnt lgkmcnt(1)
	global_store_dwordx4 v[10:11], v[0:3], off
	s_nop 1
	v_or_b32_e32 v3, 24, v12
	v_mad_u64_u32 v[0:1], s[2:3], s0, v3, 0
	v_mov_b32_e32 v2, v1
	v_mad_u64_u32 v[2:3], s[0:1], s1, v3, v[2:3]
	v_mov_b32_e32 v1, v2
	v_lshl_add_u64 v[0:1], v[0:1], 2, v[8:9]
	s_waitcnt lgkmcnt(0)
	global_store_dwordx4 v[0:1], v[4:7], off

.LBB13_5:
	v_lshlrev_b32_e32 v0, 2, v0
	v_and_b32_e32 v58, 0xfc, v0
	v_lshlrev_b64 v[4:5], 11, v[4:5]
	s_load_dwordx2 s[0:1], s[0:1], 0x8
	v_lshlrev_b32_e32 v0, 2, v58
	v_mov_b32_e32 v1, 0
	s_waitcnt lgkmcnt(0)
	v_lshl_add_u64 v[4:5], s[24:25], 0, v[4:5]
	v_lshl_add_u64 v[4:5], v[4:5], 0, v[0:1]
	global_load_dwordx4 v[8:11], v[4:5], off
	global_load_dwordx4 v[12:15], v0, s[20:21]
	global_load_dwordx4 v[16:19], v0, s[20:21] offset:1024
	global_load_dwordx4 v[20:23], v[4:5], off offset:1024
	v_lshlrev_b64 v[4:5], 11, v[2:3]
	v_lshl_add_u64 v[32:33], s[22:23], 0, v[4:5]
	v_lshl_add_u64 v[34:35], v[32:33], 0, v[0:1]
	v_lshl_add_u64 v[32:33], s[0:1], 2, v[32:33]
	global_load_dwordx4 v[24:27], v[34:35], off
	global_load_dwordx4 v[28:31], v[34:35], off offset:1024
	v_lshl_add_u64 v[40:41], v[32:33], 0, v[0:1]
	global_load_dwordx4 v[32:35], v[40:41], off
	global_load_dwordx4 v[36:39], v[40:41], off offset:1024
	global_load_dwordx4 v[44:47], v0, s[12:13] offset:1024
	v_lshlrev_b64 v[6:7], 11, v[6:7]
	global_load_dwordx4 v[40:43], v0, s[12:13]
	v_lshl_add_u64 v[6:7], s[18:19], 0, v[6:7]
	global_load_dwordx4 v[48:51], v0, s[14:15]
	v_lshl_add_u64 v[52:53], v[6:7], 0, v[0:1]
	v_mov_b32_e32 v59, 0x3727c5ac
	s_mov_b32 s12, 0xf800000
	v_mov_b32_e32 v60, 0x260
	v_lshl_add_u64 v[4:5], s[4:5], 0, v[4:5]
	v_lshlrev_b64 v[2:3], 10, v[2:3]
	s_waitcnt vmcnt(9)
	v_pk_add_f32 v[54:55], v[12:13], v[8:9]
	v_pk_add_f32 v[56:57], v[14:15], v[10:11]
	s_waitcnt vmcnt(7)
	v_pk_add_f32 v[20:21], v[16:17], v[20:21]
	v_pk_add_f32 v[18:19], v[18:19], v[22:23]
	global_load_dwordx4 v[6:9], v0, s[8:9]
	global_load_dwordx4 v[10:13], v0, s[10:11]
	global_load_dwordx4 v[14:17], v0, s[14:15] offset:1024
	s_waitcnt vmcnt(9)
	v_pk_add_f32 v[54:55], v[54:55], v[24:25]
	v_pk_add_f32 v[26:27], v[56:57], v[26:27]
	s_waitcnt vmcnt(8)
	v_pk_add_f32 v[28:29], v[20:21], v[28:29]
	v_pk_add_f32 v[30:31], v[18:19], v[30:31]
	global_load_dwordx4 v[18:21], v0, s[8:9] offset:1024
	global_load_dwordx4 v[22:25], v0, s[10:11] offset:1024
	s_waitcnt vmcnt(9)
	v_pk_add_f32 v[54:55], v[54:55], v[32:33]
	v_pk_add_f32 v[34:35], v[26:27], v[34:35]
	s_waitcnt vmcnt(8)
	v_pk_add_f32 v[36:37], v[28:29], v[36:37]
	v_pk_add_f32 v[38:39], v[30:31], v[38:39]
	global_load_dwordx4 v[26:29], v[52:53], off
	global_load_dwordx4 v[30:33], v[52:53], off offset:1024
	v_add_f32_e32 v52, 0, v54
	v_add_f32_e32 v52, v52, v55
	v_add_f32_e32 v52, v52, v34
	v_add_f32_e32 v52, v52, v35
	v_add_f32_e32 v52, v52, v36
	v_add_f32_e32 v52, v52, v37
	v_add_f32_e32 v52, v52, v38
	v_add_f32_e32 v52, v52, v39
	s_nop 1
	v_add_f32_dpp v52, v52, v52 quad_perm:[1,0,3,2] row_mask:0xf bank_mask:0xf bound_ctrl:1
	s_nop 1
	v_add_f32_dpp v52, v52, v52 quad_perm:[2,3,0,1] row_mask:0xf bank_mask:0xf bound_ctrl:1
	s_nop 1
	v_add_f32_dpp v52, v52, v52 row_half_mirror row_mask:0xf bank_mask:0xf bound_ctrl:1
	s_nop 1
	v_add_f32_dpp v52, v52, v52 row_mirror row_mask:0xf bank_mask:0xf bound_ctrl:1
	s_nop 0
	v_readlane_b32 s8, v52, 16
	v_readlane_b32 s9, v52, 48
	v_readlane_b32 s0, v52, 0
	v_readlane_b32 s1, v52, 32
	v_mov_b32_e32 v52, s8
	v_mov_b32_e32 v53, s9
	v_pk_add_f32 v[52:53], s[0:1], v[52:53]
	s_nop 0
	v_add_f32_e32 v52, v52, v53
	v_mul_f32_e32 v52, 0x3b000000, v52
	v_pk_add_f32 v[54:55], v[54:55], v[52:53] op_sel_hi:[1,0] neg_lo:[0,1] neg_hi:[0,1]
	v_pk_add_f32 v[34:35], v[34:35], v[52:53] op_sel_hi:[1,0] neg_lo:[0,1] neg_hi:[0,1]
	v_pk_add_f32 v[36:37], v[36:37], v[52:53] op_sel_hi:[1,0] neg_lo:[0,1] neg_hi:[0,1]
	v_pk_add_f32 v[38:39], v[38:39], v[52:53] op_sel_hi:[1,0] neg_lo:[0,1] neg_hi:[0,1]
	v_pk_mul_f32 v[52:53], v[54:55], v[54:55]
	s_waitcnt vmcnt(8)
	v_pk_mul_f32 v[40:41], v[40:41], v[54:55]
	v_add_f32_e32 v56, v52, v53
	v_pk_mul_f32 v[52:53], v[34:35], v[34:35]
	v_pk_mul_f32 v[34:35], v[42:43], v[34:35]
	v_add_f32_e32 v52, v56, v52
	v_add_f32_e32 v56, v52, v53
	v_pk_mul_f32 v[52:53], v[36:37], v[36:37]
	v_pk_mul_f32 v[36:37], v[44:45], v[36:37]
	v_add_f32_e32 v52, v56, v52
	v_add_f32_e32 v56, v52, v53
	v_pk_mul_f32 v[52:53], v[38:39], v[38:39]
	v_pk_mul_f32 v[38:39], v[46:47], v[38:39]
	v_add_f32_e32 v52, v56, v52
	v_add_f32_e32 v52, v52, v53
	s_nop 1
	v_add_f32_dpp v52, v52, v52 quad_perm:[1,0,3,2] row_mask:0xf bank_mask:0xf bound_ctrl:1
	s_nop 1
	v_add_f32_dpp v52, v52, v52 quad_perm:[2,3,0,1] row_mask:0xf bank_mask:0xf bound_ctrl:1
	s_nop 1
	v_add_f32_dpp v52, v52, v52 row_half_mirror row_mask:0xf bank_mask:0xf bound_ctrl:1
	s_nop 1
	v_add_f32_dpp v52, v52, v52 row_mirror row_mask:0xf bank_mask:0xf bound_ctrl:1
	s_nop 0
	v_readlane_b32 s8, v52, 16
	v_readlane_b32 s9, v52, 48
	v_readlane_b32 s0, v52, 0
	v_readlane_b32 s1, v52, 32
	v_mov_b32_e32 v52, s8
	v_mov_b32_e32 v53, s9
	v_pk_add_f32 v[52:53], s[0:1], v[52:53]
	s_nop 0
	v_add_f32_e32 v52, v52, v53
	v_fmamk_f32 v52, v52, 0x3b000000, v59
	v_mul_f32_e32 v53, 0x4f800000, v52
	v_cmp_gt_f32_e32 vcc, s12, v52
	s_nop 1
	v_cndmask_b32_e32 v52, v52, v53, vcc
	v_sqrt_f32_e32 v53, v52
	s_nop 0
	v_add_u32_e32 v42, -1, v53
	v_add_u32_e32 v43, 1, v53
	v_fma_f32 v44, -v42, v53, v52
	v_fma_f32 v45, -v43, v53, v52
	v_cmp_ge_f32_e64 s[0:1], 0, v44
	s_nop 1
	v_cndmask_b32_e64 v42, v53, v42, s[0:1]
	v_cmp_lt_f32_e64 s[0:1], 0, v45
	s_nop 1
	v_cndmask_b32_e64 v42, v42, v43, s[0:1]
	v_mul_f32_e32 v43, 0x37800000, v42
	v_cndmask_b32_e32 v42, v42, v43, vcc
	v_cmp_class_f32_e32 vcc, v52, v60
	s_nop 1
	v_cndmask_b32_e32 v42, v42, v52, vcc
	v_div_scale_f32 v43, s[0:1], v42, v42, 1.0
	v_rcp_f32_e32 v44, v43
	v_div_scale_f32 v45, vcc, 1.0, v42, 1.0
	v_fma_f32 v46, -v43, v44, 1.0
	v_fmac_f32_e32 v44, v46, v44
	v_mul_f32_e32 v46, v45, v44
	v_fma_f32 v47, -v43, v46, v45
	v_fmac_f32_e32 v46, v47, v44
	v_fma_f32 v43, -v43, v46, v45
	v_div_fmas_f32 v43, v43, v44, v46
	v_div_fixup_f32 v42, v43, v42, 1.0
	s_waitcnt vmcnt(7)
	v_pk_fma_f32 v[40:41], v[42:43], v[40:41], v[48:49] op_sel_hi:[0,1,1]
	s_waitcnt vmcnt(4)
	v_pk_fma_f32 v[14:15], v[42:43], v[36:37], v[14:15] op_sel_hi:[0,1,1]
	s_waitcnt vmcnt(1)
	v_pk_add_f32 v[26:27], v[40:41], v[26:27]
	v_pk_fma_f32 v[34:35], v[42:43], v[34:35], v[50:51] op_sel_hi:[0,1,1]
	s_waitcnt vmcnt(0)
	v_pk_add_f32 v[14:15], v[14:15], v[30:31]
	v_add_f32_e32 v30, 0, v26
	v_pk_add_f32 v[28:29], v[34:35], v[28:29]
	v_add_f32_e32 v30, v30, v27
	v_add_f32_e32 v30, v30, v28
	v_add_f32_e32 v30, v30, v29
	v_pk_fma_f32 v[16:17], v[42:43], v[38:39], v[16:17] op_sel_hi:[0,1,1]
	v_add_f32_e32 v30, v30, v14
	v_pk_add_f32 v[16:17], v[16:17], v[32:33]
	v_add_f32_e32 v30, v30, v15
	v_add_f32_e32 v30, v30, v16
	v_add_f32_e32 v30, v30, v17
	s_nop 1
	v_add_f32_dpp v30, v30, v30 quad_perm:[1,0,3,2] row_mask:0xf bank_mask:0xf bound_ctrl:1
	s_nop 1
	v_add_f32_dpp v30, v30, v30 quad_perm:[2,3,0,1] row_mask:0xf bank_mask:0xf bound_ctrl:1
	s_nop 1
	v_add_f32_dpp v30, v30, v30 row_half_mirror row_mask:0xf bank_mask:0xf bound_ctrl:1
	s_nop 1
	v_add_f32_dpp v30, v30, v30 row_mirror row_mask:0xf bank_mask:0xf bound_ctrl:1
	s_nop 0
	v_readlane_b32 s8, v30, 16
	v_readlane_b32 s9, v30, 48
	v_readlane_b32 s0, v30, 0
	v_readlane_b32 s1, v30, 32
	v_mov_b32_e32 v30, s8
	v_mov_b32_e32 v31, s9
	v_pk_add_f32 v[30:31], s[0:1], v[30:31]
	s_nop 0
	v_add_f32_e32 v30, v30, v31
	v_mul_f32_e32 v30, 0x3b000000, v30
	v_pk_add_f32 v[26:27], v[26:27], v[30:31] op_sel_hi:[1,0] neg_lo:[0,1] neg_hi:[0,1]
	v_pk_add_f32 v[28:29], v[28:29], v[30:31] op_sel_hi:[1,0] neg_lo:[0,1] neg_hi:[0,1]
	v_pk_add_f32 v[14:15], v[14:15], v[30:31] op_sel_hi:[1,0] neg_lo:[0,1] neg_hi:[0,1]
	v_pk_add_f32 v[16:17], v[16:17], v[30:31] op_sel_hi:[1,0] neg_lo:[0,1] neg_hi:[0,1]
	v_pk_mul_f32 v[30:31], v[26:27], v[26:27]
	v_pk_mul_f32 v[32:33], v[28:29], v[28:29]
	v_add_f32_e32 v30, v30, v31
	v_add_f32_e32 v30, v30, v32
	v_pk_mul_f32 v[34:35], v[14:15], v[14:15]
	v_add_f32_e32 v30, v30, v33
	v_add_f32_e32 v30, v30, v34
	v_pk_mul_f32 v[36:37], v[16:17], v[16:17]
	v_add_f32_e32 v30, v30, v35
	v_add_f32_e32 v30, v30, v36
	v_add_f32_e32 v30, v30, v37
	s_nop 1
	v_add_f32_dpp v30, v30, v30 quad_perm:[1,0,3,2] row_mask:0xf bank_mask:0xf bound_ctrl:1
	s_nop 1
	v_add_f32_dpp v30, v30, v30 quad_perm:[2,3,0,1] row_mask:0xf bank_mask:0xf bound_ctrl:1
	s_nop 1
	v_add_f32_dpp v30, v30, v30 row_half_mirror row_mask:0xf bank_mask:0xf bound_ctrl:1
	s_nop 1
	v_add_f32_dpp v30, v30, v30 row_mirror row_mask:0xf bank_mask:0xf bound_ctrl:1
	s_nop 0
	v_readlane_b32 s8, v30, 16
	v_readlane_b32 s9, v30, 48
	v_readlane_b32 s0, v30, 0
	v_readlane_b32 s1, v30, 32
	v_mov_b32_e32 v30, s8
	v_mov_b32_e32 v31, s9
	v_pk_add_f32 v[30:31], s[0:1], v[30:31]
	s_nop 0
	v_add_f32_e32 v30, v30, v31
	v_fmac_f32_e32 v59, 0x3b000000, v30
	v_mul_f32_e32 v30, 0x4f800000, v59
	v_cmp_gt_f32_e32 vcc, s12, v59
	s_nop 1
	v_cndmask_b32_e32 v30, v59, v30, vcc
	v_sqrt_f32_e32 v31, v30
	s_nop 0
	v_add_u32_e32 v32, -1, v31
	v_fma_f32 v33, -v32, v31, v30
	v_cmp_ge_f32_e64 s[0:1], 0, v33
	v_add_u32_e32 v33, 1, v31
	s_nop 0
	v_cndmask_b32_e64 v32, v31, v32, s[0:1]
	v_fma_f32 v31, -v33, v31, v30
	v_cmp_lt_f32_e64 s[0:1], 0, v31
	s_nop 1
	v_cndmask_b32_e64 v31, v32, v33, s[0:1]
	v_mul_f32_e32 v32, 0x37800000, v31
	v_cndmask_b32_e32 v31, v31, v32, vcc
	v_cmp_class_f32_e32 vcc, v30, v60
	s_nop 1
	v_cndmask_b32_e32 v32, v31, v30, vcc
	v_div_scale_f32 v33, s[0:1], v32, v32, 1.0
	v_rcp_f32_e32 v34, v33
	v_lshl_add_u64 v[30:31], v[4:5], 0, v[0:1]
	s_mov_b32 s0, 0x43000000
	v_fma_f32 v0, -v33, v34, 1.0
	v_fmac_f32_e32 v34, v0, v34
	v_div_scale_f32 v0, vcc, 1.0, v32, 1.0
	v_mul_f32_e32 v4, v0, v34
	v_fma_f32 v5, -v33, v4, v0
	v_fmac_f32_e32 v4, v5, v34
	v_fma_f32 v0, -v33, v4, v0
	v_div_fmas_f32 v0, v0, v34, v4
	v_div_fixup_f32 v0, v0, v32, 1.0
	v_pk_mul_f32 v[4:5], v[6:7], v[26:27]
	v_pk_mul_f32 v[6:7], v[8:9], v[28:29]
	v_pk_fma_f32 v[4:5], v[0:1], v[4:5], v[10:11] op_sel_hi:[0,1,1]
	v_pk_mul_f32 v[8:9], v[18:19], v[14:15]
	v_pk_fma_f32 v[6:7], v[0:1], v[6:7], v[12:13] op_sel_hi:[0,1,1]
	v_pk_fma_f32 v[8:9], v[0:1], v[8:9], v[22:23] op_sel_hi:[0,1,1]
	v_pk_mul_f32 v[10:11], v[20:21], v[16:17]
	v_fma_mixlo_f16 v12, v4, s0, 0
	v_pk_fma_f32 v[10:11], v[0:1], v[10:11], v[24:25] op_sel_hi:[0,1,1]
	global_store_dwordx4 v[30:31], v[4:7], off
	global_store_dwordx4 v[30:31], v[8:11], off offset:1024
	v_mul_f32_e32 v0, 0x43000000, v4
	v_fma_mixlo_f16 v4, v4, s0, -v12 op_sel_hi:[0,0,1]
	v_fma_mixlo_f16 v12, v8, s0, 0
	v_mul_f32_e32 v13, 0x43000000, v8
	v_fma_mixlo_f16 v8, v8, s0, -v12 op_sel_hi:[0,0,1]
	v_mul_f32_e32 v12, 0x43000000, v5
	v_fma_mixlo_f16 v14, v5, s0, 0
	v_cvt_pk_f16_f32 v12, v0, v12
	v_mul_f32_e32 v0, 0x43000000, v9
	v_pk_mul_f32 v[16:17], v[6:7], s[0:1] op_sel_hi:[1,0]
	v_fma_mixhi_f16 v4, v5, s0, -v14 op_sel_hi:[0,0,1]
	v_cvt_pk_f16_f32 v14, v13, v0
	v_cvt_pk_f16_f32 v13, v16, v17
	v_pk_mul_f32 v[18:19], v[10:11], s[0:1] op_sel_hi:[1,0]
	v_cvt_f32_f16_e32 v16, v13
	v_cvt_f32_f16_sdwa v17, v13 dst_sel:DWORD dst_unused:UNUSED_PAD src0_sel:WORD_1
	v_cvt_pk_f16_f32 v15, v18, v19
	v_cvt_f32_f16_e32 v18, v15
	v_cvt_f32_f16_sdwa v19, v15 dst_sel:DWORD dst_unused:UNUSED_PAD src0_sel:WORD_1
	v_fma_mixlo_f16 v5, v9, s0, 0
	v_pk_fma_f32 v[6:7], v[6:7], s[0:1], v[16:17] op_sel_hi:[1,0,1] neg_lo:[0,0,1] neg_hi:[0,0,1]
	v_fma_mixhi_f16 v8, v9, s0, -v5 op_sel_hi:[0,0,1]
	v_cvt_pk_f16_f32 v5, v6, v7
	v_pk_fma_f32 v[6:7], v[10:11], s[0:1], v[18:19] op_sel_hi:[1,0,1] neg_lo:[0,0,1] neg_hi:[0,0,1]
	v_lshlrev_b32_e32 v0, 1, v58
	v_cvt_pk_f16_f32 v9, v6, v7
	v_lshl_add_u64 v[6:7], s[6:7], 0, v[2:3]
	v_lshl_add_u64 v[2:3], s[2:3], 0, v[2:3]
	v_lshl_add_u64 v[6:7], v[6:7], 0, v[0:1]
	v_lshl_add_u64 v[0:1], v[2:3], 0, v[0:1]
	global_store_dwordx2 v[6:7], v[12:13], off
	global_store_dwordx2 v[6:7], v[14:15], off offset:512
	global_store_dwordx2 v[0:1], v[4:5], off
	global_store_dwordx2 v[0:1], v[8:9], off offset:512
	s_endpgm
	s_endpgm
	s_endpgm
	s_endpgm
	s_endpgm
	s_endpgm
	s_endpgm
	s_endpgm
	s_endpgm
	s_endpgm
	s_endpgm
	s_endpgm
	s_endpgm
	s_endpgm
	s_endpgm
	s_endpgm
	s_endpgm
	s_endpgm
	s_endpgm
	s_endpgm
	s_endpgm
	s_endpgm
	s_endpgm
	s_endpgm
	s_endpgm
	s_endpgm
	s_endpgm
	s_endpgm
	s_endpgm
	s_endpgm

.LBB14_5:
	v_lshlrev_b32_e32 v0, 2, v0
	v_and_b32_e32 v60, 0xfc, v0
	v_lshlrev_b64 v[8:9], 11, v[8:9]
	v_lshlrev_b32_e32 v0, 2, v60
	v_mov_b32_e32 v1, 0
	s_waitcnt lgkmcnt(0)
	v_lshl_add_u64 v[8:9], s[24:25], 0, v[8:9]
	v_lshl_add_u64 v[24:25], v[8:9], 0, v[0:1]
	global_load_dwordx4 v[8:11], v[24:25], off
	global_load_dwordx4 v[12:15], v0, s[20:21]
	global_load_dwordx4 v[16:19], v0, s[20:21] offset:1024
	global_load_dwordx4 v[20:23], v[24:25], off offset:1024
	s_load_dwordx2 s[0:1], s[0:1], 0x8
	v_lshlrev_b64 v[4:5], 11, v[2:3]
	v_lshl_add_u64 v[36:37], s[22:23], 0, v[4:5]
	v_lshl_add_u64 v[28:29], v[36:37], 0, v[0:1]
	global_load_dwordx4 v[24:27], v[28:29], off
	s_waitcnt lgkmcnt(0)
	v_lshl_add_u64 v[30:31], s[0:1], 2, v[36:37]
	v_lshl_add_u64 v[38:39], v[30:31], 0, v[0:1]
	v_lshl_add_u64 v[32:33], s[0:1], 3, v[36:37]
	v_lshl_add_u64 v[44:45], v[32:33], 0, v[0:1]
	global_load_dwordx4 v[32:35], v[38:39], off
	v_mad_u64_u32 v[48:49], s[16:17], s0, 12, v[36:37]
	global_load_dwordx4 v[28:31], v[28:29], off offset:1024
	v_mov_b32_e32 v40, v49
	v_mad_u64_u32 v[46:47], s[0:1], s1, 12, v[40:41]
	global_load_dwordx4 v[40:43], v[44:45], off
	v_mov_b32_e32 v49, v46
	v_lshl_add_u64 v[56:57], v[48:49], 0, v[0:1]
	global_load_dwordx4 v[36:39], v[38:39], off offset:1024
	v_lshlrev_b64 v[6:7], 11, v[6:7]
	global_load_dwordx4 v[44:47], v[44:45], off offset:1024
	s_nop 0
	global_load_dwordx4 v[48:51], v[56:57], off
	global_load_dwordx4 v[52:55], v[56:57], off offset:1024
	v_lshl_add_u64 v[6:7], s[18:19], 0, v[6:7]
	v_lshl_add_u64 v[56:57], v[6:7], 0, v[0:1]
	v_mov_b32_e32 v61, 0x3727c5ac
	s_mov_b32 s16, 0xf800000
	v_lshl_add_u64 v[4:5], s[4:5], 0, v[4:5]
	v_lshlrev_b64 v[2:3], 10, v[2:3]
	s_waitcnt vmcnt(10)
	v_pk_add_f32 v[58:59], v[12:13], v[8:9]
	v_pk_add_f32 v[14:15], v[14:15], v[10:11]
	global_load_dwordx4 v[6:9], v0, s[12:13]
	global_load_dwordx4 v[10:13], v0, s[14:15]
	s_waitcnt vmcnt(10)
	v_pk_add_f32 v[16:17], v[16:17], v[20:21]
	v_pk_add_f32 v[18:19], v[18:19], v[22:23]
	s_waitcnt vmcnt(9)
	v_pk_add_f32 v[22:23], v[58:59], v[24:25]
	v_pk_add_f32 v[24:25], v[14:15], v[26:27]
	s_waitcnt vmcnt(8)
	v_pk_add_f32 v[32:33], v[22:23], v[32:33]
	v_pk_add_f32 v[34:35], v[24:25], v[34:35]
	s_waitcnt vmcnt(7)
	v_pk_add_f32 v[58:59], v[16:17], v[28:29]
	v_pk_add_f32 v[30:31], v[18:19], v[30:31]
	global_load_dwordx4 v[14:17], v0, s[12:13] offset:1024
	global_load_dwordx4 v[18:21], v0, s[14:15] offset:1024
	global_load_dwordx4 v[22:25], v[56:57], off
	global_load_dwordx4 v[26:29], v[56:57], off offset:1024
	s_waitcnt vmcnt(10)
	v_pk_add_f32 v[32:33], v[32:33], v[40:41]
	v_pk_add_f32 v[34:35], v[34:35], v[42:43]
	s_waitcnt vmcnt(9)
	v_pk_add_f32 v[30:31], v[30:31], v[38:39]
	v_pk_add_f32 v[36:37], v[58:59], v[36:37]
	s_waitcnt vmcnt(7)
	v_pk_add_f32 v[32:33], v[32:33], v[48:49]
	v_pk_add_f32 v[34:35], v[34:35], v[50:51]
	v_add_f32_e32 v38, 0, v32
	v_add_f32_e32 v38, v38, v33
	v_pk_add_f32 v[36:37], v[36:37], v[44:45]
	v_add_f32_e32 v38, v38, v34
	s_waitcnt vmcnt(6)
	v_pk_add_f32 v[36:37], v[36:37], v[52:53]
	v_add_f32_e32 v38, v38, v35
	v_pk_add_f32 v[30:31], v[30:31], v[46:47]
	v_add_f32_e32 v38, v38, v36
	v_pk_add_f32 v[30:31], v[30:31], v[54:55]
	v_add_f32_e32 v38, v38, v37
	v_add_f32_e32 v38, v38, v30
	v_add_f32_e32 v38, v38, v31
	v_mov_b32_e32 v55, 0x260
	s_nop 0
	v_add_f32_dpp v38, v38, v38 quad_perm:[1,0,3,2] row_mask:0xf bank_mask:0xf bound_ctrl:1
	s_nop 1
	v_add_f32_dpp v38, v38, v38 quad_perm:[2,3,0,1] row_mask:0xf bank_mask:0xf bound_ctrl:1
	s_nop 1
	v_add_f32_dpp v38, v38, v38 row_half_mirror row_mask:0xf bank_mask:0xf bound_ctrl:1
	s_nop 1
	v_add_f32_dpp v38, v38, v38 row_mirror row_mask:0xf bank_mask:0xf bound_ctrl:1
	s_nop 0
	v_readlane_b32 s12, v38, 16
	v_readlane_b32 s13, v38, 48
	v_readlane_b32 s0, v38, 0
	v_readlane_b32 s1, v38, 32
	v_mov_b32_e32 v38, s12
	v_mov_b32_e32 v39, s13
	v_pk_add_f32 v[38:39], s[0:1], v[38:39]
	s_nop 0
	v_add_f32_e32 v38, v38, v39
	v_mul_f32_e32 v38, 0x3b000000, v38
	v_pk_add_f32 v[46:47], v[32:33], v[38:39] op_sel_hi:[1,0] neg_lo:[0,1] neg_hi:[0,1]
	v_pk_add_f32 v[48:49], v[34:35], v[38:39] op_sel_hi:[1,0] neg_lo:[0,1] neg_hi:[0,1]
	v_pk_add_f32 v[52:53], v[30:31], v[38:39] op_sel_hi:[1,0] neg_lo:[0,1] neg_hi:[0,1]
	v_pk_mul_f32 v[30:31], v[46:47], v[46:47]
	v_pk_mul_f32 v[32:33], v[48:49], v[48:49]
	v_add_f32_e32 v30, v30, v31
	v_pk_add_f32 v[50:51], v[36:37], v[38:39] op_sel_hi:[1,0] neg_lo:[0,1] neg_hi:[0,1]
	v_add_f32_e32 v30, v30, v32
	v_pk_mul_f32 v[34:35], v[50:51], v[50:51]
	v_add_f32_e32 v30, v30, v33
	v_add_f32_e32 v30, v30, v34
	v_pk_mul_f32 v[36:37], v[52:53], v[52:53]
	v_add_f32_e32 v30, v30, v35
	v_add_f32_e32 v30, v30, v36
	v_add_f32_e32 v30, v30, v37
	s_waitcnt vmcnt(5)
	v_pk_mul_f32 v[6:7], v[6:7], v[46:47]
	v_add_f32_dpp v30, v30, v30 quad_perm:[1,0,3,2] row_mask:0xf bank_mask:0xf bound_ctrl:1
	v_pk_mul_f32 v[8:9], v[8:9], v[48:49]
	s_nop 0
	v_add_f32_dpp v30, v30, v30 quad_perm:[2,3,0,1] row_mask:0xf bank_mask:0xf bound_ctrl:1
	s_nop 1
	v_add_f32_dpp v30, v30, v30 row_half_mirror row_mask:0xf bank_mask:0xf bound_ctrl:1
	s_nop 1
	v_add_f32_dpp v30, v30, v30 row_mirror row_mask:0xf bank_mask:0xf bound_ctrl:1
	s_nop 0
	v_readlane_b32 s12, v30, 16
	v_readlane_b32 s13, v30, 48
	v_readlane_b32 s0, v30, 0
	v_readlane_b32 s1, v30, 32
	v_mov_b32_e32 v30, s12
	v_mov_b32_e32 v31, s13
	v_pk_add_f32 v[30:31], s[0:1], v[30:31]
	s_nop 0
	v_add_f32_e32 v30, v30, v31
	v_fmamk_f32 v30, v30, 0x3b000000, v61
	v_mul_f32_e32 v31, 0x4f800000, v30
	v_cmp_gt_f32_e32 vcc, s16, v30
	s_nop 1
	v_cndmask_b32_e32 v54, v30, v31, vcc
	v_sqrt_f32_e32 v38, v54
	global_load_dwordx4 v[30:33], v0, s[8:9]
	global_load_dwordx4 v[34:37], v0, s[10:11]
	v_add_u32_e32 v39, -1, v38
	v_add_u32_e32 v56, 1, v38
	v_fma_f32 v40, -v39, v38, v54
	v_fma_f32 v41, -v56, v38, v54
	v_cmp_ge_f32_e64 s[0:1], 0, v40
	s_nop 1
	v_cndmask_b32_e64 v57, v38, v39, s[0:1]
	v_cmp_lt_f32_e64 s[0:1], 0, v41
	global_load_dwordx4 v[38:41], v0, s[8:9] offset:1024
	global_load_dwordx4 v[42:45], v0, s[10:11] offset:1024
	v_cndmask_b32_e64 v46, v57, v56, s[0:1]
	v_mul_f32_e32 v47, 0x37800000, v46
	v_cndmask_b32_e32 v46, v46, v47, vcc
	v_cmp_class_f32_e32 vcc, v54, v55
	s_nop 1
	v_cndmask_b32_e32 v46, v46, v54, vcc
	v_div_scale_f32 v47, s[0:1], v46, v46, 1.0
	v_rcp_f32_e32 v54, v47
	v_div_scale_f32 v48, vcc, 1.0, v46, 1.0
	v_fma_f32 v49, -v47, v54, 1.0
	v_fmac_f32_e32 v54, v49, v54
	v_mul_f32_e32 v49, v48, v54
	v_fma_f32 v56, -v47, v49, v48
	v_fmac_f32_e32 v49, v56, v54
	v_fma_f32 v47, -v47, v49, v48
	v_div_fmas_f32 v47, v47, v54, v49
	v_div_fixup_f32 v46, v47, v46, 1.0
	s_waitcnt vmcnt(8)
	v_pk_fma_f32 v[6:7], v[46:47], v[6:7], v[10:11] op_sel_hi:[0,1,1]
	s_waitcnt vmcnt(5)
	v_pk_add_f32 v[6:7], v[6:7], v[22:23]
	v_pk_fma_f32 v[8:9], v[46:47], v[8:9], v[12:13] op_sel_hi:[0,1,1]
	v_pk_mul_f32 v[10:11], v[14:15], v[50:51]
	v_add_f32_e32 v14, 0, v6
	v_add_f32_e32 v14, v14, v7
	v_pk_add_f32 v[8:9], v[8:9], v[24:25]
	v_pk_fma_f32 v[10:11], v[46:47], v[10:11], v[18:19] op_sel_hi:[0,1,1]
	v_add_f32_e32 v14, v14, v8
	v_pk_mul_f32 v[12:13], v[16:17], v[52:53]
	v_add_f32_e32 v14, v14, v9
	s_waitcnt vmcnt(4)
	v_pk_add_f32 v[10:11], v[10:11], v[26:27]
	v_pk_fma_f32 v[12:13], v[46:47], v[12:13], v[20:21] op_sel_hi:[0,1,1]
	v_add_f32_e32 v14, v14, v10
	v_add_f32_e32 v14, v14, v11
	v_pk_add_f32 v[12:13], v[12:13], v[28:29]
	s_nop 0
	v_add_f32_e32 v14, v14, v12
	v_add_f32_e32 v14, v14, v13
	s_nop 1
	v_add_f32_dpp v14, v14, v14 quad_perm:[1,0,3,2] row_mask:0xf bank_mask:0xf bound_ctrl:1
	s_nop 1
	v_add_f32_dpp v14, v14, v14 quad_perm:[2,3,0,1] row_mask:0xf bank_mask:0xf bound_ctrl:1
	s_nop 1
	v_add_f32_dpp v14, v14, v14 row_half_mirror row_mask:0xf bank_mask:0xf bound_ctrl:1
	s_nop 1
	v_add_f32_dpp v14, v14, v14 row_mirror row_mask:0xf bank_mask:0xf bound_ctrl:1
	s_nop 0
	v_readlane_b32 s8, v14, 16
	v_readlane_b32 s9, v14, 48
	v_readlane_b32 s0, v14, 0
	v_readlane_b32 s1, v14, 32
	v_mov_b32_e32 v14, s8
	v_mov_b32_e32 v15, s9
	v_pk_add_f32 v[14:15], s[0:1], v[14:15]
	s_nop 0
	v_add_f32_e32 v14, v14, v15
	v_mul_f32_e32 v14, 0x3b000000, v14
	v_pk_add_f32 v[6:7], v[6:7], v[14:15] op_sel_hi:[1,0] neg_lo:[0,1] neg_hi:[0,1]
	v_pk_add_f32 v[8:9], v[8:9], v[14:15] op_sel_hi:[1,0] neg_lo:[0,1] neg_hi:[0,1]
	v_pk_mul_f32 v[16:17], v[6:7], v[6:7]
	v_pk_mul_f32 v[18:19], v[8:9], v[8:9]
	v_add_f32_e32 v16, v16, v17
	v_pk_add_f32 v[10:11], v[10:11], v[14:15] op_sel_hi:[1,0] neg_lo:[0,1] neg_hi:[0,1]
	v_add_f32_e32 v16, v16, v18
	v_pk_mul_f32 v[20:21], v[10:11], v[10:11]
	v_add_f32_e32 v16, v16, v19
	v_pk_add_f32 v[12:13], v[12:13], v[14:15] op_sel_hi:[1,0] neg_lo:[0,1] neg_hi:[0,1]
	v_add_f32_e32 v16, v16, v20
	v_pk_mul_f32 v[14:15], v[12:13], v[12:13]
	v_add_f32_e32 v16, v16, v21
	v_add_f32_e32 v14, v16, v14
	v_add_f32_e32 v14, v14, v15
	s_nop 1
	v_add_f32_dpp v14, v14, v14 quad_perm:[1,0,3,2] row_mask:0xf bank_mask:0xf bound_ctrl:1
	s_nop 1
	v_add_f32_dpp v14, v14, v14 quad_perm:[2,3,0,1] row_mask:0xf bank_mask:0xf bound_ctrl:1
	s_nop 1
	v_add_f32_dpp v14, v14, v14 row_half_mirror row_mask:0xf bank_mask:0xf bound_ctrl:1
	s_nop 1
	v_add_f32_dpp v14, v14, v14 row_mirror row_mask:0xf bank_mask:0xf bound_ctrl:1
	s_nop 0
	v_readlane_b32 s8, v14, 16
	v_readlane_b32 s9, v14, 48
	v_readlane_b32 s0, v14, 0
	v_readlane_b32 s1, v14, 32
	v_mov_b32_e32 v14, s8
	v_mov_b32_e32 v15, s9
	v_pk_add_f32 v[14:15], s[0:1], v[14:15]
	s_nop 0
	v_add_f32_e32 v14, v14, v15
	v_fmac_f32_e32 v61, 0x3b000000, v14
	v_mul_f32_e32 v14, 0x4f800000, v61
	v_cmp_gt_f32_e32 vcc, s16, v61
	s_nop 1
	v_cndmask_b32_e32 v14, v61, v14, vcc
	v_sqrt_f32_e32 v15, v14
	s_nop 0
	v_add_u32_e32 v16, -1, v15
	v_fma_f32 v17, -v16, v15, v14
	v_cmp_ge_f32_e64 s[0:1], 0, v17
	v_add_u32_e32 v17, 1, v15
	s_nop 0
	v_cndmask_b32_e64 v16, v15, v16, s[0:1]
	v_fma_f32 v15, -v17, v15, v14
	v_cmp_lt_f32_e64 s[0:1], 0, v15
	s_nop 1
	v_cndmask_b32_e64 v15, v16, v17, s[0:1]
	v_mul_f32_e32 v16, 0x37800000, v15
	v_cndmask_b32_e32 v15, v15, v16, vcc
	v_cmp_class_f32_e32 vcc, v14, v55
	s_nop 1
	v_cndmask_b32_e32 v16, v15, v14, vcc
	v_div_scale_f32 v17, s[0:1], v16, v16, 1.0
	v_rcp_f32_e32 v18, v17
	v_lshl_add_u64 v[14:15], v[4:5], 0, v[0:1]
	s_mov_b32 s0, 0x43000000
	v_fma_f32 v0, -v17, v18, 1.0
	v_fmac_f32_e32 v18, v0, v18
	v_div_scale_f32 v0, vcc, 1.0, v16, 1.0
	v_mul_f32_e32 v4, v0, v18
	v_fma_f32 v5, -v17, v4, v0
	v_fmac_f32_e32 v4, v5, v18
	v_fma_f32 v0, -v17, v4, v0
	v_div_fmas_f32 v0, v0, v18, v4
	v_div_fixup_f32 v0, v0, v16, 1.0
	s_waitcnt vmcnt(3)
	v_pk_mul_f32 v[4:5], v[30:31], v[6:7]
	v_pk_mul_f32 v[6:7], v[32:33], v[8:9]
	s_waitcnt vmcnt(2)
	v_pk_fma_f32 v[4:5], v[0:1], v[4:5], v[34:35] op_sel_hi:[0,1,1]
	s_waitcnt vmcnt(1)
	v_pk_mul_f32 v[8:9], v[38:39], v[10:11]
	v_pk_fma_f32 v[6:7], v[0:1], v[6:7], v[36:37] op_sel_hi:[0,1,1]
	s_waitcnt vmcnt(0)
	v_pk_fma_f32 v[8:9], v[0:1], v[8:9], v[42:43] op_sel_hi:[0,1,1]
	v_pk_mul_f32 v[10:11], v[40:41], v[12:13]
	v_fma_mixlo_f16 v12, v4, s0, 0
	v_pk_fma_f32 v[10:11], v[0:1], v[10:11], v[44:45] op_sel_hi:[0,1,1]
	global_store_dwordx4 v[14:15], v[4:7], off
	global_store_dwordx4 v[14:15], v[8:11], off offset:1024
	v_mul_f32_e32 v0, 0x43000000, v4
	v_fma_mixlo_f16 v4, v4, s0, -v12 op_sel_hi:[0,0,1]
	v_fma_mixlo_f16 v12, v8, s0, 0
	v_mul_f32_e32 v13, 0x43000000, v8
	v_fma_mixlo_f16 v8, v8, s0, -v12 op_sel_hi:[0,0,1]
	v_mul_f32_e32 v12, 0x43000000, v5
	v_fma_mixlo_f16 v14, v5, s0, 0
	v_cvt_pk_f16_f32 v12, v0, v12
	v_mul_f32_e32 v0, 0x43000000, v9
	v_pk_mul_f32 v[16:17], v[6:7], s[0:1] op_sel_hi:[1,0]
	v_fma_mixhi_f16 v4, v5, s0, -v14 op_sel_hi:[0,0,1]
	v_cvt_pk_f16_f32 v14, v13, v0
	v_cvt_pk_f16_f32 v13, v16, v17
	v_pk_mul_f32 v[18:19], v[10:11], s[0:1] op_sel_hi:[1,0]
	v_cvt_f32_f16_e32 v16, v13
	v_cvt_f32_f16_sdwa v17, v13 dst_sel:DWORD dst_unused:UNUSED_PAD src0_sel:WORD_1
	v_cvt_pk_f16_f32 v15, v18, v19
	v_cvt_f32_f16_e32 v18, v15
	v_cvt_f32_f16_sdwa v19, v15 dst_sel:DWORD dst_unused:UNUSED_PAD src0_sel:WORD_1
	v_fma_mixlo_f16 v5, v9, s0, 0
	v_pk_fma_f32 v[6:7], v[6:7], s[0:1], v[16:17] op_sel_hi:[1,0,1] neg_lo:[0,0,1] neg_hi:[0,0,1]
	v_fma_mixhi_f16 v8, v9, s0, -v5 op_sel_hi:[0,0,1]
	v_cvt_pk_f16_f32 v5, v6, v7
	v_pk_fma_f32 v[6:7], v[10:11], s[0:1], v[18:19] op_sel_hi:[1,0,1] neg_lo:[0,0,1] neg_hi:[0,0,1]
	v_lshlrev_b32_e32 v0, 1, v60
	v_cvt_pk_f16_f32 v9, v6, v7
	v_lshl_add_u64 v[6:7], s[6:7], 0, v[2:3]
	v_lshl_add_u64 v[2:3], s[2:3], 0, v[2:3]
	v_lshl_add_u64 v[6:7], v[6:7], 0, v[0:1]
	v_lshl_add_u64 v[0:1], v[2:3], 0, v[0:1]
	global_store_dwordx2 v[6:7], v[12:13], off
	global_store_dwordx2 v[6:7], v[14:15], off offset:512
	global_store_dwordx2 v[0:1], v[4:5], off
	global_store_dwordx2 v[0:1], v[8:9], off offset:512
	s_endpgm
	s_endpgm
	s_endpgm
	s_endpgm
	s_endpgm
	s_endpgm
	s_endpgm
	s_endpgm
	s_endpgm
	s_endpgm
	s_endpgm
	s_endpgm
	s_endpgm
	s_endpgm
	s_endpgm
	s_endpgm
	s_endpgm
	s_endpgm
	s_endpgm
	s_endpgm
	s_endpgm
	s_endpgm
	s_endpgm
	s_endpgm
	s_endpgm
	s_endpgm
	s_endpgm
	s_endpgm
	s_endpgm
	s_endpgm
	s_endpgm
	s_endpgm
	s_endpgm
	s_endpgm
	s_endpgm
	s_endpgm
	s_endpgm
	s_endpgm
	s_endpgm
	s_endpgm
	s_endpgm
	s_endpgm
	s_endpgm
	s_endpgm
	s_endpgm
	s_endpgm
	s_endpgm
	s_endpgm
	s_endpgm
	s_endpgm
	s_endpgm
	s_endpgm

.LBB15_5:
	v_lshlrev_b32_e32 v0, 2, v0
	v_and_b32_e32 v8, 0xfc, v0
	v_lshlrev_b64 v[4:5], 11, v[4:5]
	v_lshlrev_b32_e32 v0, 2, v8
	v_mov_b32_e32 v1, 0
	s_waitcnt lgkmcnt(0)
	v_lshl_add_u64 v[4:5], s[24:25], 0, v[4:5]
	v_lshl_add_u64 v[4:5], v[4:5], 0, v[0:1]
	global_load_dwordx4 v[10:13], v[4:5], off
	global_load_dwordx4 v[14:17], v0, s[20:21]
	global_load_dwordx4 v[18:21], v0, s[20:21] offset:1024
	global_load_dwordx4 v[22:25], v[4:5], off offset:1024
	s_load_dwordx2 s[0:1], s[0:1], 0x8
	v_lshlrev_b64 v[4:5], 11, v[2:3]
	v_lshl_add_u64 v[50:51], s[22:23], 0, v[4:5]
	v_lshl_add_u64 v[30:31], v[50:51], 0, v[0:1]
	global_load_dwordx4 v[26:29], v[30:31], off
	s_waitcnt lgkmcnt(0)
	v_lshl_add_u64 v[34:35], s[0:1], 2, v[50:51]
	global_load_dwordx4 v[30:33], v[30:31], off offset:1024
	v_lshl_add_u64 v[42:43], v[34:35], 0, v[0:1]
	global_load_dwordx4 v[34:37], v[42:43], off
	global_load_dwordx4 v[38:41], v[42:43], off offset:1024
	v_lshl_add_u64 v[42:43], s[0:1], 3, v[50:51]
	v_lshl_add_u64 v[52:53], v[42:43], 0, v[0:1]
	global_load_dwordx4 v[42:45], v[52:53], off
	global_load_dwordx4 v[46:49], v[52:53], off offset:1024
	v_mad_u64_u32 v[52:53], s[16:17], s0, 12, v[50:51]
	v_mad_u64_u32 v[56:57], s[16:17], s0, 20, v[50:51]
	v_mad_u64_u32 v[62:63], s[16:17], s0, 24, v[50:51]
	v_lshl_add_u64 v[54:55], s[0:1], 4, v[50:51]
	v_mad_u64_u32 v[50:51], s[16:17], s0, 28, v[50:51]
	v_lshl_add_u64 v[54:55], v[54:55], 0, v[0:1]
	v_lshlrev_b64 v[6:7], 11, v[6:7]
	v_lshl_add_u64 v[6:7], s[18:19], 0, v[6:7]
	v_lshl_add_u64 v[6:7], v[6:7], 0, v[0:1]
	v_lshl_add_u64 v[4:5], s[4:5], 0, v[4:5]
	v_lshlrev_b64 v[2:3], 10, v[2:3]
	s_waitcnt vmcnt(8)
	v_pk_add_f32 v[58:59], v[14:15], v[10:11]
	v_mov_b32_e32 v10, v53
	v_pk_add_f32 v[60:61], v[16:17], v[12:13]
	v_mov_b32_e32 v12, v57
	v_mad_u64_u32 v[10:11], s[16:17], s1, 12, v[10:11]
	v_mov_b32_e32 v53, v10
	v_mov_b32_e32 v10, v63
	v_mad_u64_u32 v[12:13], s[16:17], s1, 20, v[12:13]
	v_mov_b32_e32 v57, v12
	v_mov_b32_e32 v12, v51
	v_mad_u64_u32 v[10:11], s[16:17], s1, 24, v[10:11]
	s_waitcnt vmcnt(6)
	v_pk_add_f32 v[66:67], v[18:19], v[22:23]
	v_lshl_add_u64 v[22:23], v[52:53], 0, v[0:1]
	v_mad_u64_u32 v[64:65], s[0:1], s1, 28, v[12:13]
	v_mov_b32_e32 v63, v10
	v_pk_add_f32 v[68:69], v[20:21], v[24:25]
	global_load_dwordx4 v[10:13], v[54:55], off
	global_load_dwordx4 v[14:17], v[54:55], off offset:1024
	global_load_dwordx4 v[18:21], v[22:23], off
	v_lshl_add_u64 v[52:53], v[56:57], 0, v[0:1]
	s_waitcnt vmcnt(8)
	v_pk_add_f32 v[54:55], v[58:59], v[26:27]
	v_pk_add_f32 v[56:57], v[60:61], v[28:29]
	global_load_dwordx4 v[26:29], v[52:53], off
	v_lshl_add_u64 v[58:59], v[62:63], 0, v[0:1]
	global_load_dwordx4 v[22:25], v[22:23], off offset:1024
	v_mov_b32_e32 v51, v64
	s_waitcnt vmcnt(9)
	v_pk_add_f32 v[60:61], v[66:67], v[30:31]
	v_pk_add_f32 v[62:63], v[68:69], v[32:33]
	s_waitcnt vmcnt(8)
	v_pk_add_f32 v[54:55], v[54:55], v[34:35]
	v_pk_add_f32 v[56:57], v[56:57], v[36:37]
	global_load_dwordx4 v[30:33], v[52:53], off offset:1024
	global_load_dwordx4 v[34:37], v[58:59], off
	v_lshl_add_u64 v[50:51], v[50:51], 0, v[0:1]
	s_waitcnt vmcnt(9)
	v_pk_add_f32 v[52:53], v[60:61], v[38:39]
	v_pk_add_f32 v[60:61], v[62:63], v[40:41]
	s_waitcnt vmcnt(8)
	v_pk_add_f32 v[54:55], v[54:55], v[42:43]
	v_pk_add_f32 v[56:57], v[56:57], v[44:45]
	global_load_dwordx4 v[38:41], v[50:51], off
	global_load_dwordx4 v[42:45], v[58:59], off offset:1024
	s_waitcnt vmcnt(9)
	v_pk_add_f32 v[52:53], v[52:53], v[46:47]
	v_pk_add_f32 v[58:59], v[60:61], v[48:49]
	global_load_dwordx4 v[46:49], v[50:51], off offset:1024
	s_waitcnt vmcnt(7)
	v_pk_add_f32 v[18:19], v[54:55], v[18:19]
	s_nop 0
	v_pk_add_f32 v[10:11], v[18:19], v[10:11]
	v_pk_add_f32 v[20:21], v[56:57], v[20:21]
	v_mov_b32_e32 v57, 0x3727c5ac
	s_waitcnt vmcnt(6)
	v_pk_add_f32 v[18:19], v[10:11], v[26:27]
	v_pk_add_f32 v[12:13], v[20:21], v[12:13]
	s_waitcnt vmcnt(5)
	v_pk_add_f32 v[22:23], v[52:53], v[22:23]
	v_pk_add_f32 v[10:11], v[58:59], v[24:25]
	v_pk_add_f32 v[14:15], v[22:23], v[14:15]
	v_pk_add_f32 v[10:11], v[10:11], v[16:17]
	v_pk_add_f32 v[20:21], v[12:13], v[28:29]
	v_mov_b32_e32 v58, 0x260
	s_waitcnt vmcnt(4)
	v_pk_add_f32 v[50:51], v[14:15], v[30:31]
	v_pk_add_f32 v[52:53], v[10:11], v[32:33]
	global_load_dwordx4 v[10:13], v0, s[12:13]
	global_load_dwordx4 v[14:17], v0, s[14:15]
	s_waitcnt vmcnt(5)
	v_pk_add_f32 v[18:19], v[18:19], v[34:35]
	s_waitcnt vmcnt(4)
	v_pk_add_f32 v[34:35], v[18:19], v[38:39]
	v_pk_add_f32 v[18:19], v[20:21], v[36:37]
	v_add_f32_e32 v9, 0, v34
	v_pk_add_f32 v[36:37], v[18:19], v[40:41]
	global_load_dwordx4 v[18:21], v0, s[12:13] offset:1024
	global_load_dwordx4 v[22:25], v0, s[14:15] offset:1024
	global_load_dwordx4 v[26:29], v[6:7], off
	global_load_dwordx4 v[30:33], v[6:7], off offset:1024
	v_add_f32_e32 v9, v9, v35
	v_add_f32_e32 v9, v9, v36
	s_waitcnt vmcnt(7)
	v_pk_add_f32 v[6:7], v[50:51], v[42:43]
	v_add_f32_e32 v9, v9, v37
	s_waitcnt vmcnt(6)
	v_pk_add_f32 v[6:7], v[6:7], v[46:47]
	v_pk_add_f32 v[38:39], v[52:53], v[44:45]
	v_add_f32_e32 v9, v9, v6
	v_add_f32_e32 v9, v9, v7
	v_pk_add_f32 v[38:39], v[38:39], v[48:49]
	s_nop 0
	v_add_f32_e32 v9, v9, v38
	v_add_f32_e32 v9, v9, v39
	s_nop 1
	v_add_f32_dpp v9, v9, v9 quad_perm:[1,0,3,2] row_mask:0xf bank_mask:0xf bound_ctrl:1
	s_nop 1
	v_add_f32_dpp v9, v9, v9 quad_perm:[2,3,0,1] row_mask:0xf bank_mask:0xf bound_ctrl:1
	s_nop 1
	v_add_f32_dpp v9, v9, v9 row_half_mirror row_mask:0xf bank_mask:0xf bound_ctrl:1
	s_nop 1
	v_add_f32_dpp v9, v9, v9 row_mirror row_mask:0xf bank_mask:0xf bound_ctrl:1
	s_nop 0
	v_readlane_b32 s12, v9, 16
	v_readlane_b32 s13, v9, 48
	v_readlane_b32 s0, v9, 0
	v_readlane_b32 s1, v9, 32
	v_mov_b32_e32 v40, s12
	v_mov_b32_e32 v41, s13
	v_pk_add_f32 v[40:41], s[0:1], v[40:41]
	s_nop 0
	v_add_f32_e32 v9, v40, v41
	v_mul_f32_e32 v40, 0x3b000000, v9
	v_pk_add_f32 v[50:51], v[34:35], v[40:41] op_sel_hi:[1,0] neg_lo:[0,1] neg_hi:[0,1]
	v_pk_add_f32 v[52:53], v[36:37], v[40:41] op_sel_hi:[1,0] neg_lo:[0,1] neg_hi:[0,1]
	v_pk_mul_f32 v[34:35], v[50:51], v[50:51]
	v_pk_mul_f32 v[36:37], v[52:53], v[52:53]
	v_add_f32_e32 v9, v34, v35
	v_pk_add_f32 v[6:7], v[6:7], v[40:41] op_sel_hi:[1,0] neg_lo:[0,1] neg_hi:[0,1]
	v_add_f32_e32 v9, v9, v36
	v_pk_mul_f32 v[42:43], v[6:7], v[6:7]
	v_add_f32_e32 v9, v9, v37
	v_pk_add_f32 v[54:55], v[38:39], v[40:41] op_sel_hi:[1,0] neg_lo:[0,1] neg_hi:[0,1]
	v_add_f32_e32 v9, v9, v42
	v_pk_mul_f32 v[38:39], v[54:55], v[54:55]
	v_add_f32_e32 v9, v9, v43
	v_add_f32_e32 v9, v9, v38
	v_add_f32_e32 v9, v9, v39
	s_waitcnt vmcnt(5)
	v_pk_mul_f32 v[10:11], v[10:11], v[50:51]
	v_add_f32_dpp v9, v9, v9 quad_perm:[1,0,3,2] row_mask:0xf bank_mask:0xf bound_ctrl:1
	v_pk_mul_f32 v[12:13], v[12:13], v[52:53]
	s_waitcnt vmcnt(3)
	v_pk_mul_f32 v[6:7], v[18:19], v[6:7]
	v_add_f32_dpp v9, v9, v9 quad_perm:[2,3,0,1] row_mask:0xf bank_mask:0xf bound_ctrl:1
	s_nop 1
	v_add_f32_dpp v9, v9, v9 row_half_mirror row_mask:0xf bank_mask:0xf bound_ctrl:1
	s_nop 1
	v_add_f32_dpp v9, v9, v9 row_mirror row_mask:0xf bank_mask:0xf bound_ctrl:1
	s_nop 0
	v_readlane_b32 s12, v9, 16
	v_readlane_b32 s13, v9, 48
	v_readlane_b32 s0, v9, 0
	v_readlane_b32 s1, v9, 32
	v_mov_b32_e32 v34, s12
	v_mov_b32_e32 v35, s13
	v_pk_add_f32 v[34:35], s[0:1], v[34:35]
	s_mov_b32 s12, 0xf800000
	v_add_f32_e32 v9, v34, v35
	v_fmamk_f32 v9, v9, 0x3b000000, v57
	v_mul_f32_e32 v34, 0x4f800000, v9
	v_cmp_gt_f32_e32 vcc, s12, v9
	s_nop 1
	v_cndmask_b32_e32 v9, v9, v34, vcc
	v_sqrt_f32_e32 v34, v9
	s_nop 0
	v_add_u32_e32 v35, -1, v34
	v_fma_f32 v36, -v35, v34, v9
	v_cmp_ge_f32_e64 s[0:1], 0, v36
	v_add_u32_e32 v36, 1, v34
	s_nop 0
	v_cndmask_b32_e64 v35, v34, v35, s[0:1]
	v_fma_f32 v34, -v36, v34, v9
	v_cmp_lt_f32_e64 s[0:1], 0, v34
	s_nop 1
	v_cndmask_b32_e64 v34, v35, v36, s[0:1]
	v_mul_f32_e32 v35, 0x37800000, v34
	v_cndmask_b32_e32 v34, v34, v35, vcc
	v_cmp_class_f32_e32 vcc, v9, v58
	s_nop 1
	v_cndmask_b32_e32 v9, v34, v9, vcc
	v_div_scale_f32 v42, s[0:1], v9, v9, 1.0
	v_rcp_f32_e32 v43, v42
	global_load_dwordx4 v[34:37], v0, s[8:9]
	global_load_dwordx4 v[38:41], v0, s[10:11]
	v_fma_f32 v44, -v42, v43, 1.0
	v_fmac_f32_e32 v43, v44, v43
	v_div_scale_f32 v44, vcc, 1.0, v9, 1.0
	v_mul_f32_e32 v45, v44, v43
	v_fma_f32 v46, -v42, v45, v44
	v_fmac_f32_e32 v45, v46, v43
	v_fma_f32 v42, -v42, v45, v44
	v_div_fmas_f32 v56, v42, v43, v45
	global_load_dwordx4 v[42:45], v0, s[8:9] offset:1024
	global_load_dwordx4 v[46:49], v0, s[10:11] offset:1024
	v_div_fixup_f32 v56, v56, v9, 1.0
	v_pk_fma_f32 v[10:11], v[56:57], v[10:11], v[14:15] op_sel_hi:[0,1,1]
	s_waitcnt vmcnt(5)
	v_pk_add_f32 v[10:11], v[10:11], v[26:27]
	v_pk_fma_f32 v[12:13], v[56:57], v[12:13], v[16:17] op_sel_hi:[0,1,1]
	v_add_f32_e32 v9, 0, v10
	v_add_f32_e32 v9, v9, v11
	v_pk_add_f32 v[12:13], v[12:13], v[28:29]
	v_pk_fma_f32 v[6:7], v[56:57], v[6:7], v[22:23] op_sel_hi:[0,1,1]
	v_add_f32_e32 v9, v9, v12
	v_pk_mul_f32 v[14:15], v[20:21], v[54:55]
	v_add_f32_e32 v9, v9, v13
	s_waitcnt vmcnt(4)
	v_pk_add_f32 v[6:7], v[6:7], v[30:31]
	v_pk_fma_f32 v[14:15], v[56:57], v[14:15], v[24:25] op_sel_hi:[0,1,1]
	v_add_f32_e32 v9, v9, v6
	v_add_f32_e32 v9, v9, v7
	v_pk_add_f32 v[14:15], v[14:15], v[32:33]
	s_nop 0
	v_add_f32_e32 v9, v9, v14
	v_add_f32_e32 v9, v9, v15
	s_nop 1
	v_add_f32_dpp v9, v9, v9 quad_perm:[1,0,3,2] row_mask:0xf bank_mask:0xf bound_ctrl:1
	s_nop 1
	v_add_f32_dpp v9, v9, v9 quad_perm:[2,3,0,1] row_mask:0xf bank_mask:0xf bound_ctrl:1
	s_nop 1
	v_add_f32_dpp v9, v9, v9 row_half_mirror row_mask:0xf bank_mask:0xf bound_ctrl:1
	s_nop 1
	v_add_f32_dpp v9, v9, v9 row_mirror row_mask:0xf bank_mask:0xf bound_ctrl:1
	s_nop 0
	v_readlane_b32 s8, v9, 16
	v_readlane_b32 s9, v9, 48
	v_readlane_b32 s0, v9, 0
	v_readlane_b32 s1, v9, 32
	v_mov_b32_e32 v16, s8
	v_mov_b32_e32 v17, s9
	v_pk_add_f32 v[16:17], s[0:1], v[16:17]
	s_nop 0
	v_add_f32_e32 v9, v16, v17
	v_mul_f32_e32 v16, 0x3b000000, v9
	v_pk_add_f32 v[10:11], v[10:11], v[16:17] op_sel_hi:[1,0] neg_lo:[0,1] neg_hi:[0,1]
	v_pk_add_f32 v[12:13], v[12:13], v[16:17] op_sel_hi:[1,0] neg_lo:[0,1] neg_hi:[0,1]
	v_pk_mul_f32 v[18:19], v[10:11], v[10:11]
	v_pk_mul_f32 v[20:21], v[12:13], v[12:13]
	v_add_f32_e32 v9, v18, v19
	v_pk_add_f32 v[22:23], v[6:7], v[16:17] op_sel_hi:[1,0] neg_lo:[0,1] neg_hi:[0,1]
	v_add_f32_e32 v9, v9, v20
	v_pk_mul_f32 v[6:7], v[22:23], v[22:23]
	v_add_f32_e32 v9, v9, v21
	v_pk_add_f32 v[14:15], v[14:15], v[16:17] op_sel_hi:[1,0] neg_lo:[0,1] neg_hi:[0,1]
	v_add_f32_e32 v6, v9, v6
	v_pk_mul_f32 v[16:17], v[14:15], v[14:15]
	v_add_f32_e32 v6, v6, v7
	v_add_f32_e32 v6, v6, v16
	v_add_f32_e32 v6, v6, v17
	s_nop 1
	v_add_f32_dpp v6, v6, v6 quad_perm:[1,0,3,2] row_mask:0xf bank_mask:0xf bound_ctrl:1
	s_nop 1
	v_add_f32_dpp v6, v6, v6 quad_perm:[2,3,0,1] row_mask:0xf bank_mask:0xf bound_ctrl:1
	s_nop 1
	v_add_f32_dpp v6, v6, v6 row_half_mirror row_mask:0xf bank_mask:0xf bound_ctrl:1
	s_nop 1
	v_add_f32_dpp v6, v6, v6 row_mirror row_mask:0xf bank_mask:0xf bound_ctrl:1
	s_nop 0
	v_readlane_b32 s8, v6, 16
	v_readlane_b32 s9, v6, 48
	v_readlane_b32 s0, v6, 0
	v_readlane_b32 s1, v6, 32
	v_mov_b32_e32 v6, s8
	v_mov_b32_e32 v7, s9
	v_pk_add_f32 v[6:7], s[0:1], v[6:7]
	s_nop 0
	v_add_f32_e32 v6, v6, v7
	v_fmac_f32_e32 v57, 0x3b000000, v6
	v_mul_f32_e32 v6, 0x4f800000, v57
	v_cmp_gt_f32_e32 vcc, s12, v57
	s_nop 1
	v_cndmask_b32_e32 v6, v57, v6, vcc
	v_sqrt_f32_e32 v7, v6
	s_nop 0
	v_add_u32_e32 v9, -1, v7
	v_fma_f32 v16, -v9, v7, v6
	v_cmp_ge_f32_e64 s[0:1], 0, v16
	v_add_u32_e32 v16, 1, v7
	s_nop 0
	v_cndmask_b32_e64 v9, v7, v9, s[0:1]
	v_fma_f32 v7, -v16, v7, v6
	v_cmp_lt_f32_e64 s[0:1], 0, v7
	s_nop 1
	v_cndmask_b32_e64 v7, v9, v16, s[0:1]
	v_mul_f32_e32 v9, 0x37800000, v7
	v_cndmask_b32_e32 v7, v7, v9, vcc
	v_cmp_class_f32_e32 vcc, v6, v58
	v_lshl_add_u64 v[16:17], v[4:5], 0, v[0:1]
	s_nop 0
	v_cndmask_b32_e32 v6, v7, v6, vcc
	v_div_scale_f32 v7, s[0:1], v6, v6, 1.0
	v_rcp_f32_e32 v9, v7
	s_mov_b32 s0, 0x43000000
	v_fma_f32 v0, -v7, v9, 1.0
	v_fmac_f32_e32 v9, v0, v9
	v_div_scale_f32 v0, vcc, 1.0, v6, 1.0
	v_mul_f32_e32 v4, v0, v9
	v_fma_f32 v5, -v7, v4, v0
	v_fmac_f32_e32 v4, v5, v9
	v_fma_f32 v0, -v7, v4, v0
	v_div_fmas_f32 v0, v0, v9, v4
	v_div_fixup_f32 v0, v0, v6, 1.0
	s_waitcnt vmcnt(3)
	v_pk_mul_f32 v[4:5], v[34:35], v[10:11]
	v_pk_mul_f32 v[6:7], v[36:37], v[12:13]
	s_waitcnt vmcnt(2)
	v_pk_fma_f32 v[4:5], v[0:1], v[4:5], v[38:39] op_sel_hi:[0,1,1]
	v_pk_fma_f32 v[6:7], v[0:1], v[6:7], v[40:41] op_sel_hi:[0,1,1]
	s_waitcnt vmcnt(1)
	v_pk_mul_f32 v[10:11], v[42:43], v[22:23]
	v_pk_mul_f32 v[12:13], v[44:45], v[14:15]
	v_fma_mixlo_f16 v9, v4, s0, 0
	s_waitcnt vmcnt(0)
	v_pk_fma_f32 v[10:11], v[0:1], v[10:11], v[46:47] op_sel_hi:[0,1,1]
	v_pk_fma_f32 v[12:13], v[0:1], v[12:13], v[48:49] op_sel_hi:[0,1,1]
	global_store_dwordx4 v[16:17], v[4:7], off
	global_store_dwordx4 v[16:17], v[10:13], off offset:1024
	v_mul_f32_e32 v0, 0x43000000, v4
	v_fma_mixlo_f16 v4, v4, s0, -v9 op_sel_hi:[0,0,1]
	v_fma_mixlo_f16 v15, v5, s0, 0
	v_pk_mul_f32 v[18:19], v[6:7], s[0:1] op_sel_hi:[1,0]
	v_fma_mixhi_f16 v4, v5, s0, -v15 op_sel_hi:[0,0,1]
	v_cvt_pk_f16_f32 v15, v18, v19
	v_pk_mul_f32 v[20:21], v[12:13], s[0:1] op_sel_hi:[1,0]
	v_cvt_f32_f16_e32 v18, v15
	v_cvt_f32_f16_sdwa v19, v15 dst_sel:DWORD dst_unused:UNUSED_PAD src0_sel:WORD_1
	v_cvt_pk_f16_f32 v17, v20, v21
	v_cvt_f32_f16_e32 v20, v17
	v_cvt_f32_f16_sdwa v21, v17 dst_sel:DWORD dst_unused:UNUSED_PAD src0_sel:WORD_1
	v_fma_mixlo_f16 v14, v10, s0, 0
	v_mul_f32_e32 v9, 0x43000000, v10
	v_fma_mixlo_f16 v10, v10, s0, -v14 op_sel_hi:[0,0,1]
	v_mul_f32_e32 v14, 0x43000000, v5
	v_fma_mixlo_f16 v5, v11, s0, 0
	v_pk_fma_f32 v[6:7], v[6:7], s[0:1], v[18:19] op_sel_hi:[1,0,1] neg_lo:[0,0,1] neg_hi:[0,0,1]
	v_cvt_pk_f16_f32 v14, v0, v14
	v_mul_f32_e32 v0, 0x43000000, v11
	v_fma_mixhi_f16 v10, v11, s0, -v5 op_sel_hi:[0,0,1]
	v_cvt_pk_f16_f32 v5, v6, v7
	v_pk_fma_f32 v[6:7], v[12:13], s[0:1], v[20:21] op_sel_hi:[1,0,1] neg_lo:[0,0,1] neg_hi:[0,0,1]
	v_cvt_pk_f16_f32 v16, v9, v0
	v_cvt_pk_f16_f32 v11, v6, v7
	v_lshl_add_u64 v[6:7], s[6:7], 0, v[2:3]
	v_lshlrev_b32_e32 v0, 1, v8
	v_lshl_add_u64 v[2:3], s[2:3], 0, v[2:3]
	v_lshl_add_u64 v[6:7], v[6:7], 0, v[0:1]
	v_lshl_add_u64 v[0:1], v[2:3], 0, v[0:1]
	global_store_dwordx2 v[6:7], v[14:15], off
	global_store_dwordx2 v[6:7], v[16:17], off offset:512
	global_store_dwordx2 v[0:1], v[4:5], off
	global_store_dwordx2 v[0:1], v[10:11], off offset:512
	s_endpgm
	s_endpgm
	s_endpgm
	s_endpgm
	s_endpgm
	s_endpgm
	s_endpgm
	s_endpgm
	s_endpgm
	s_endpgm
	s_endpgm
	s_endpgm
	s_endpgm
	s_endpgm
	s_endpgm
	s_endpgm
	s_endpgm
	s_endpgm
	s_endpgm
	s_endpgm
	s_endpgm
	s_endpgm
	s_endpgm
	s_endpgm
	s_endpgm
	s_endpgm
	s_endpgm
	s_endpgm
	s_endpgm
	s_endpgm
	s_endpgm
	s_endpgm

.LBB18_9:
	s_waitcnt vmcnt(7)
	s_nop 7
	v_accvgpr_read_b32 v21, a1
	v_mul_u32_u24_e32 v14, 0xa0, v14
	s_waitcnt vmcnt(6)
	v_accvgpr_read_b32 v22, a0
	v_or_b32_e32 v13, v14, v13
	v_fma_f32 v14, s6, v21, v12
	v_lshrrev_b32_e32 v23, 6, v0
	v_fma_f32 v22, s6, v22, v12
	s_mov_b32 s3, 0x43800000
	v_max_f32_e32 v14, 0, v14
	v_mul_u32_u24_e32 v23, 0x1400, v23
	v_max_f32_e32 v22, 0, v22
	v_fma_mixlo_f16 v21, v14, s3, 0
	v_accvgpr_read_b32 v20, a2
	v_fma_mixlo_f16 v24, v22, s3, 0
	v_lshl_or_b32 v13, v13, 1, v23
	v_fma_mixlo_f16 v14, v14, s3, -v21 op_sel_hi:[0,0,1]
	s_load_dwordx4 s[8:11], s[0:1], 0x50
	v_fma_mixlo_f16 v22, v22, s3, -v24 op_sel_hi:[0,0,1]
	s_load_dwordx2 s[0:1], s[0:1], 0x40
	s_waitcnt lgkmcnt(0)
	s_barrier
	ds_write_b16 v13, v24
	ds_write_b16 v13, v22 offset:2560
	ds_write_b16 v13, v21 offset:80
	ds_write_b16 v13, v14 offset:2640
	v_fma_f32 v14, s6, v20, v12
	v_max_f32_e32 v14, 0, v14
	v_fma_mixlo_f16 v20, v14, s3, 0
	v_accvgpr_read_b32 v19, a3
	v_fma_mixlo_f16 v14, v14, s3, -v20 op_sel_hi:[0,0,1]
	ds_write_b16 v13, v20 offset:160
	ds_write_b16 v13, v14 offset:2720
	v_fma_f32 v14, s6, v19, v12
	v_max_f32_e32 v14, 0, v14
	v_fma_mixlo_f16 v19, v14, s3, 0
	v_accvgpr_read_b32 v18, a4
	v_fma_mixlo_f16 v14, v14, s3, -v19 op_sel_hi:[0,0,1]
	ds_write_b16 v13, v19 offset:240
	ds_write_b16 v13, v14 offset:2800
	v_fma_f32 v14, s6, v18, v12
	v_max_f32_e32 v14, 0, v14
	v_fma_mixlo_f16 v18, v14, s3, 0
	v_accvgpr_read_b32 v17, a5
	v_fma_mixlo_f16 v14, v14, s3, -v18 op_sel_hi:[0,0,1]
	ds_write_b16 v13, v18 offset:640
	ds_write_b16 v13, v14 offset:3200
	v_fma_f32 v14, s6, v17, v12
	v_max_f32_e32 v14, 0, v14
	v_fma_mixlo_f16 v17, v14, s3, 0
	v_accvgpr_read_b32 v16, a6
	v_fma_mixlo_f16 v14, v14, s3, -v17 op_sel_hi:[0,0,1]
	ds_write_b16 v13, v17 offset:720
	ds_write_b16 v13, v14 offset:3280
	v_fma_f32 v14, s6, v16, v12
	v_max_f32_e32 v14, 0, v14
	v_fma_mixlo_f16 v16, v14, s3, 0
	v_accvgpr_read_b32 v15, a7
	v_fma_mixlo_f16 v14, v14, s3, -v16 op_sel_hi:[0,0,1]
	ds_write_b16 v13, v16 offset:800
	ds_write_b16 v13, v14 offset:3360
	v_fma_f32 v14, s6, v15, v12
	v_accvgpr_read_b32 v11, a8
	v_max_f32_e32 v14, 0, v14
	v_fma_mixlo_f16 v15, v14, s3, 0
	v_fma_f32 v11, s6, v11, v12
	v_accvgpr_read_b32 v10, a9
	v_fma_mixlo_f16 v14, v14, s3, -v15 op_sel_hi:[0,0,1]
	v_max_f32_e32 v11, 0, v11
	ds_write_b16 v13, v15 offset:880
	ds_write_b16 v13, v14 offset:3440
	v_fma_mixlo_f16 v14, v11, s3, 0
	v_fma_f32 v10, s6, v10, v12
	v_accvgpr_read_b32 v9, a10
	v_fma_mixlo_f16 v11, v11, s3, -v14 op_sel_hi:[0,0,1]
	v_max_f32_e32 v10, 0, v10
	ds_write_b16 v13, v14 offset:1280
	ds_write_b16 v13, v11 offset:3840
	v_fma_mixlo_f16 v11, v10, s3, 0
	v_fma_f32 v9, s6, v9, v12
	v_accvgpr_read_b32 v8, a11
	v_fma_mixlo_f16 v10, v10, s3, -v11 op_sel_hi:[0,0,1]
	v_max_f32_e32 v9, 0, v9
	ds_write_b16 v13, v11 offset:1360
	ds_write_b16 v13, v10 offset:3920
	v_fma_mixlo_f16 v10, v9, s3, 0
	v_fma_f32 v8, s6, v8, v12
	v_accvgpr_read_b32 v7, a12
	v_fma_mixlo_f16 v9, v9, s3, -v10 op_sel_hi:[0,0,1]
	v_max_f32_e32 v8, 0, v8
	ds_write_b16 v13, v10 offset:1440
	ds_write_b16 v13, v9 offset:4000
	v_fma_mixlo_f16 v9, v8, s3, 0
	v_fma_f32 v7, s6, v7, v12
	v_accvgpr_read_b32 v6, a13
	v_fma_mixlo_f16 v8, v8, s3, -v9 op_sel_hi:[0,0,1]
	v_max_f32_e32 v7, 0, v7
	ds_write_b16 v13, v9 offset:1520
	ds_write_b16 v13, v8 offset:4080
	v_fma_mixlo_f16 v8, v7, s3, 0
	v_fma_f32 v6, s6, v6, v12
	v_accvgpr_read_b32 v5, a14
	v_fma_mixlo_f16 v7, v7, s3, -v8 op_sel_hi:[0,0,1]
	v_max_f32_e32 v6, 0, v6
	ds_write_b16 v13, v8 offset:1920
	ds_write_b16 v13, v7 offset:4480
	v_fma_mixlo_f16 v7, v6, s3, 0
	v_fma_f32 v5, s6, v5, v12
	v_accvgpr_read_b32 v4, a15
	v_fma_mixlo_f16 v6, v6, s3, -v7 op_sel_hi:[0,0,1]
	v_max_f32_e32 v5, 0, v5
	ds_write_b16 v13, v7 offset:2000
	ds_write_b16 v13, v6 offset:4560
	v_fma_mixlo_f16 v6, v5, s3, 0
	v_fmac_f32_e32 v12, s6, v4
	v_fma_mixlo_f16 v5, v5, s3, -v6 op_sel_hi:[0,0,1]
	v_max_f32_e32 v4, 0, v12
	ds_write_b16 v13, v6 offset:2080
	ds_write_b16 v13, v5 offset:4640
	v_fma_mixlo_f16 v5, v4, s3, 0
	v_and_b32_e32 v0, 63, v0
	v_fma_mixlo_f16 v4, v4, s3, -v5 op_sel_hi:[0,0,1]
	v_add_u32_e32 v3, s2, v3
	s_ashr_i32 s2, s7, 31
	ds_write_b16 v13, v5 offset:2160
	ds_write_b16 v13, v4 offset:4720
	v_lshrrev_b32_e32 v20, 2, v0
	v_ashrrev_i32_e32 v4, 31, v3
	v_or3_b32 v0, v1, v2, s7
	v_mov_b32_e32 v1, s2
	v_mul_lo_u32 v4, s0, v4
	v_mad_u64_u32 v[0:1], s[2:3], s0, v3, v[0:1]
	v_mul_lo_u32 v3, s1, v3
	v_add3_u32 v1, v3, v1, v4
	v_lshlrev_b64 v[0:1], 1, v[0:1]
	v_lshl_or_b32 v2, v2, 1, v23
	v_lshl_add_u64 v[12:13], s[8:9], 0, v[0:1]
	v_lshl_add_u64 v[14:15], s[10:11], 0, v[0:1]
	v_mul_u32_u24_e32 v0, 40, v20
	v_lshl_add_u32 v21, v0, 1, v2
	v_mad_u64_u32 v[8:9], s[2:3], s0, v20, 0
	ds_read_b128 v[0:3], v21
	ds_read_b128 v[4:7], v21 offset:2560
	v_mov_b32_e32 v10, v9
	v_mad_u64_u32 v[10:11], s[2:3], s1, v20, v[10:11]
	v_mov_b32_e32 v9, v10
	v_lshlrev_b64 v[16:17], 1, v[8:9]
	v_lshl_add_u64 v[18:19], v[12:13], 0, v[16:17]
	v_lshl_add_u64 v[16:17], v[14:15], 0, v[16:17]
	s_waitcnt lgkmcnt(0)
	global_store_dwordx4 v[16:17], v[4:7], off
	ds_read_b128 v[8:11], v21 offset:1280
	global_store_dwordx4 v[18:19], v[0:3], off
	v_or_b32_e32 v7, 16, v20
	v_mad_u64_u32 v[4:5], s[2:3], s0, v7, 0
	ds_read_b128 v[0:3], v21 offset:3840
	v_mov_b32_e32 v6, v5
	v_mad_u64_u32 v[6:7], s[0:1], s1, v7, v[6:7]
	v_mov_b32_e32 v5, v6
	v_lshlrev_b64 v[4:5], 1, v[4:5]
	v_lshl_add_u64 v[6:7], v[12:13], 0, v[4:5]
	v_lshl_add_u64 v[4:5], v[14:15], 0, v[4:5]
	s_waitcnt lgkmcnt(1)
	global_store_dwordx4 v[6:7], v[8:11], off
	s_waitcnt lgkmcnt(0)
	global_store_dwordx4 v[4:5], v[0:3], off
	s_endpgm
	s_endpgm
	s_endpgm
	s_endpgm
	s_endpgm
	s_endpgm
	s_endpgm
	s_endpgm
	s_endpgm
	s_endpgm
	s_endpgm
	s_endpgm
	s_endpgm
	s_endpgm
	s_endpgm
	s_endpgm
	s_endpgm
	s_endpgm
	s_endpgm
	s_endpgm
	s_endpgm
	s_endpgm
	s_endpgm
	s_endpgm
	s_endpgm
	s_endpgm
	s_endpgm
	s_endpgm
	s_endpgm
	s_endpgm
	s_endpgm
	s_endpgm
	s_endpgm
	s_endpgm
	s_endpgm
	s_endpgm
	s_endpgm
	s_endpgm
	s_endpgm
	s_endpgm
	s_endpgm
	s_endpgm
	s_endpgm
	s_endpgm
	s_endpgm
	s_endpgm

.LBB19_5:
	v_lshlrev_b32_e32 v0, 2, v0
	v_and_b32_e32 v50, 0xfc, v0
	v_lshlrev_b64 v[2:3], 11, v[2:3]
	v_lshlrev_b32_e32 v4, 2, v50
	v_mov_b32_e32 v5, 0
	s_waitcnt lgkmcnt(0)
	v_lshl_add_u64 v[2:3], s[14:15], 0, v[2:3]
	v_lshlrev_b64 v[36:37], 11, v[6:7]
	v_lshl_add_u64 v[2:3], v[2:3], 0, v[4:5]
	v_lshl_add_u64 v[0:1], s[18:19], 0, v[36:37]
	global_load_dwordx4 v[8:11], v[2:3], off
	global_load_dwordx4 v[12:15], v4, s[16:17]
	global_load_dwordx4 v[16:19], v4, s[16:17] offset:1024
	global_load_dwordx4 v[20:23], v[2:3], off offset:1024
	v_lshl_add_u64 v[38:39], v[0:1], 0, v[4:5]
	global_load_dwordx4 v[24:27], v[38:39], off
	global_load_dwordx4 v[28:31], v[38:39], off offset:1024
	global_load_dwordx4 v[32:35], v4, s[4:5]
	global_load_dwordx4 v[0:3], v4, s[4:5] offset:1024
	v_lshl_add_u64 v[36:37], s[8:9], 0, v[36:37]
	v_lshl_add_u64 v[48:49], v[36:37], 0, v[4:5]
	global_load_dwordx4 v[36:39], v4, s[6:7]
	global_load_dwordx4 v[40:43], v4, s[6:7] offset:1024
	v_lshlrev_b64 v[6:7], 10, v[6:7]
	v_lshl_add_u64 v[44:45], s[10:11], 0, v[6:7]
	v_lshl_add_u64 v[46:47], s[2:3], 0, v[6:7]
	v_mov_b32_e32 v51, 0x3727c5ac
	s_mov_b32 s5, 0xf800000
	v_mov_b32_e32 v52, 0x260
	s_mov_b32 s4, 0x43000000
	v_lshlrev_b32_e32 v4, 1, v50
	v_lshl_add_u64 v[44:45], v[44:45], 0, v[4:5]
	s_waitcnt vmcnt(8)
	v_pk_add_f32 v[6:7], v[12:13], v[8:9]
	s_waitcnt vmcnt(5)
	v_pk_add_f32 v[6:7], v[24:25], v[6:7]
	v_pk_add_f32 v[8:9], v[14:15], v[10:11]
	v_add_f32_e32 v14, 0, v6
	v_pk_add_f32 v[8:9], v[26:27], v[8:9]
	v_add_f32_e32 v14, v14, v7
	v_pk_add_f32 v[10:11], v[16:17], v[20:21]
	v_add_f32_e32 v14, v14, v8
	s_waitcnt vmcnt(4)
	v_pk_add_f32 v[10:11], v[28:29], v[10:11]
	v_add_f32_e32 v14, v14, v9
	v_pk_add_f32 v[12:13], v[18:19], v[22:23]
	v_add_f32_e32 v14, v14, v10
	v_pk_add_f32 v[12:13], v[30:31], v[12:13]
	v_add_f32_e32 v14, v14, v11
	v_add_f32_e32 v14, v14, v12
	v_add_f32_e32 v14, v14, v13
	s_nop 1
	v_add_f32_dpp v14, v14, v14 quad_perm:[1,0,3,2] row_mask:0xf bank_mask:0xf bound_ctrl:1
	s_nop 1
	v_add_f32_dpp v14, v14, v14 quad_perm:[2,3,0,1] row_mask:0xf bank_mask:0xf bound_ctrl:1
	s_nop 1
	v_add_f32_dpp v14, v14, v14 row_half_mirror row_mask:0xf bank_mask:0xf bound_ctrl:1
	s_nop 1
	v_add_f32_dpp v14, v14, v14 row_mirror row_mask:0xf bank_mask:0xf bound_ctrl:1
	s_nop 0
	v_readlane_b32 s2, v14, 16
	v_readlane_b32 s3, v14, 48
	v_readlane_b32 s0, v14, 0
	v_readlane_b32 s1, v14, 32
	v_mov_b32_e32 v14, s2
	v_mov_b32_e32 v15, s3
	v_pk_add_f32 v[14:15], s[0:1], v[14:15]
	s_nop 0
	v_add_f32_e32 v14, v14, v15
	v_mul_f32_e32 v14, 0x3b000000, v14
	v_pk_add_f32 v[6:7], v[6:7], v[14:15] op_sel_hi:[1,0] neg_lo:[0,1] neg_hi:[0,1]
	v_pk_add_f32 v[8:9], v[8:9], v[14:15] op_sel_hi:[1,0] neg_lo:[0,1] neg_hi:[0,1]
	v_pk_add_f32 v[10:11], v[10:11], v[14:15] op_sel_hi:[1,0] neg_lo:[0,1] neg_hi:[0,1]
	v_pk_add_f32 v[12:13], v[12:13], v[14:15] op_sel_hi:[1,0] neg_lo:[0,1] neg_hi:[0,1]
	v_pk_mul_f32 v[14:15], v[6:7], v[6:7]
	v_pk_mul_f32 v[16:17], v[8:9], v[8:9]
	v_add_f32_e32 v14, v14, v15
	v_add_f32_e32 v14, v14, v16
	v_pk_mul_f32 v[18:19], v[10:11], v[10:11]
	v_add_f32_e32 v14, v14, v17
	v_add_f32_e32 v14, v14, v18
	v_pk_mul_f32 v[20:21], v[12:13], v[12:13]
	v_add_f32_e32 v14, v14, v19
	v_add_f32_e32 v14, v14, v20
	v_add_f32_e32 v14, v14, v21
	s_waitcnt vmcnt(2)
	v_pk_mul_f32 v[10:11], v[0:1], v[10:11]
	v_pk_mul_f32 v[12:13], v[2:3], v[12:13]
	v_add_f32_dpp v14, v14, v14 quad_perm:[1,0,3,2] row_mask:0xf bank_mask:0xf bound_ctrl:1
	v_pk_mul_f32 v[6:7], v[32:33], v[6:7]
	v_pk_mul_f32 v[8:9], v[34:35], v[8:9]
	v_add_f32_dpp v14, v14, v14 quad_perm:[2,3,0,1] row_mask:0xf bank_mask:0xf bound_ctrl:1
	s_nop 1
	v_add_f32_dpp v14, v14, v14 row_half_mirror row_mask:0xf bank_mask:0xf bound_ctrl:1
	s_nop 1
	v_add_f32_dpp v14, v14, v14 row_mirror row_mask:0xf bank_mask:0xf bound_ctrl:1
	s_nop 0
	v_readlane_b32 s2, v14, 16
	v_readlane_b32 s3, v14, 48
	v_readlane_b32 s0, v14, 0
	v_readlane_b32 s1, v14, 32
	v_mov_b32_e32 v14, s2
	v_mov_b32_e32 v15, s3
	v_pk_add_f32 v[14:15], s[0:1], v[14:15]
	s_nop 0
	v_add_f32_e32 v14, v14, v15
	v_fmac_f32_e32 v51, 0x3b000000, v14
	v_mul_f32_e32 v14, 0x4f800000, v51
	v_cmp_gt_f32_e32 vcc, s5, v51
	s_nop 1
	v_cndmask_b32_e32 v14, v51, v14, vcc
	v_sqrt_f32_e32 v15, v14
	s_nop 0
	v_add_u32_e32 v0, -1, v15
	v_add_u32_e32 v1, 1, v15
	v_fma_f32 v16, -v0, v15, v14
	v_fma_f32 v17, -v1, v15, v14
	v_cmp_ge_f32_e64 s[0:1], 0, v16
	s_nop 1
	v_cndmask_b32_e64 v0, v15, v0, s[0:1]
	v_cmp_lt_f32_e64 s[0:1], 0, v17
	s_nop 1
	v_cndmask_b32_e64 v0, v0, v1, s[0:1]
	v_mul_f32_e32 v1, 0x37800000, v0
	v_cndmask_b32_e32 v0, v0, v1, vcc
	v_cmp_class_f32_e32 vcc, v14, v52
	s_nop 1
	v_cndmask_b32_e32 v0, v0, v14, vcc
	v_div_scale_f32 v1, s[0:1], v0, v0, 1.0
	v_rcp_f32_e32 v14, v1
	v_div_scale_f32 v2, vcc, 1.0, v0, 1.0
	v_fma_f32 v3, -v1, v14, 1.0
	v_fmac_f32_e32 v14, v3, v14
	v_mul_f32_e32 v3, v2, v14
	v_fma_f32 v15, -v1, v3, v2
	v_fmac_f32_e32 v3, v15, v14
	v_fma_f32 v1, -v1, v3, v2
	v_div_fmas_f32 v1, v1, v14, v3
	v_div_fixup_f32 v14, v1, v0, 1.0
	s_waitcnt vmcnt(1)
	v_pk_fma_f32 v[0:1], v[14:15], v[6:7], v[36:37] op_sel_hi:[0,1,1]
	v_pk_fma_f32 v[2:3], v[14:15], v[8:9], v[38:39] op_sel_hi:[0,1,1]
	s_waitcnt vmcnt(0)
	v_pk_fma_f32 v[6:7], v[14:15], v[10:11], v[40:41] op_sel_hi:[0,1,1]
	v_pk_fma_f32 v[8:9], v[14:15], v[12:13], v[42:43] op_sel_hi:[0,1,1]
	v_fma_mixlo_f16 v15, v0, s4, 0
	v_pk_mul_f32 v[10:11], v[2:3], s[4:5] op_sel_hi:[1,0]
	global_store_dwordx4 v[48:49], v[0:3], off
	global_store_dwordx4 v[48:49], v[6:9], off offset:1024
	v_mul_f32_e32 v14, 0x43000000, v0
	v_fma_mixlo_f16 v17, v6, s4, 0
	v_pk_mul_f32 v[12:13], v[8:9], s[4:5] op_sel_hi:[1,0]
	v_fma_mixlo_f16 v0, v0, s4, -v15 op_sel_hi:[0,0,1]
	v_cvt_pk_f16_f32 v15, v10, v11
	v_mul_f32_e32 v16, 0x43000000, v6
	v_fma_mixlo_f16 v6, v6, s4, -v17 op_sel_hi:[0,0,1]
	v_cvt_pk_f16_f32 v17, v12, v13
	v_cvt_f32_f16_e32 v10, v15
	v_cvt_f32_f16_sdwa v11, v15 dst_sel:DWORD dst_unused:UNUSED_PAD src0_sel:WORD_1
	v_cvt_f32_f16_e32 v12, v17
	v_cvt_f32_f16_sdwa v13, v17 dst_sel:DWORD dst_unused:UNUSED_PAD src0_sel:WORD_1
	v_mul_f32_e32 v18, 0x43000000, v1
	v_fma_mixlo_f16 v19, v1, s4, 0
	v_pk_fma_f32 v[2:3], v[2:3], s[4:5], v[10:11] op_sel_hi:[1,0,1] neg_lo:[0,0,1] neg_hi:[0,0,1]
	v_mul_f32_e32 v20, 0x43000000, v7
	v_fma_mixlo_f16 v21, v7, s4, 0
	v_cvt_pk_f16_f32 v14, v14, v18
	v_fma_mixhi_f16 v0, v1, s4, -v19 op_sel_hi:[0,0,1]
	v_pk_fma_f32 v[8:9], v[8:9], s[4:5], v[12:13] op_sel_hi:[1,0,1] neg_lo:[0,0,1] neg_hi:[0,0,1]
	v_cvt_pk_f16_f32 v1, v2, v3
	v_lshl_add_u64 v[2:3], v[46:47], 0, v[4:5]
	v_cvt_pk_f16_f32 v16, v16, v20
	v_fma_mixhi_f16 v6, v7, s4, -v21 op_sel_hi:[0,0,1]
	global_store_dwordx2 v[44:45], v[14:15], off
	global_store_dwordx2 v[44:45], v[16:17], off offset:512
	v_cvt_pk_f16_f32 v7, v8, v9
	global_store_dwordx2 v[2:3], v[0:1], off
	global_store_dwordx2 v[2:3], v[6:7], off offset:512
	s_endpgm
	s_endpgm
	s_endpgm
	s_endpgm
	s_endpgm
	s_endpgm
	s_endpgm
	s_endpgm
	s_endpgm
	s_endpgm
	s_endpgm
	s_endpgm
	s_endpgm
	s_endpgm
	s_endpgm

.LBB21_5:
	v_lshlrev_b32_e32 v0, 2, v0
	v_and_b32_e32 v58, 0xfc, v0
	v_lshlrev_b64 v[4:5], 11, v[4:5]
	v_lshlrev_b32_e32 v0, 2, v58
	v_mov_b32_e32 v1, 0
	s_waitcnt lgkmcnt(0)
	v_lshl_add_u64 v[4:5], s[18:19], 0, v[4:5]
	v_lshl_add_u64 v[20:21], v[4:5], 0, v[0:1]
	global_load_dwordx4 v[4:7], v[20:21], off
	global_load_dwordx4 v[8:11], v0, s[16:17]
	global_load_dwordx4 v[12:15], v0, s[16:17] offset:1024
	global_load_dwordx4 v[16:19], v[20:21], off offset:1024
	s_load_dwordx2 s[0:1], s[0:1], 0x8
	v_lshlrev_b64 v[52:53], 11, v[2:3]
	v_lshl_add_u64 v[28:29], s[14:15], 0, v[52:53]
	v_lshl_add_u64 v[24:25], v[28:29], 0, v[0:1]
	v_mov_b32_e32 v59, 0x3727c5ac
	s_waitcnt lgkmcnt(0)
	v_lshl_add_u64 v[20:21], s[0:1], 2, v[28:29]
	v_lshl_add_u64 v[26:27], s[0:1], 3, v[28:29]
	v_lshl_add_u64 v[36:37], v[20:21], 0, v[0:1]
	global_load_dwordx4 v[20:23], v[24:25], off
	v_lshl_add_u64 v[40:41], v[26:27], 0, v[0:1]
	global_load_dwordx4 v[24:27], v[24:25], off offset:1024
	v_mad_u64_u32 v[44:45], s[12:13], s0, 12, v[28:29]
	v_mov_b32_e32 v38, v45
	v_mad_u64_u32 v[42:43], s[0:1], s1, 12, v[38:39]
	global_load_dwordx4 v[28:31], v[36:37], off
	global_load_dwordx4 v[32:35], v[36:37], off offset:1024
	v_mov_b32_e32 v45, v42
	global_load_dwordx4 v[36:39], v[40:41], off
	v_lshl_add_u64 v[54:55], v[44:45], 0, v[0:1]
	global_load_dwordx4 v[40:43], v[40:41], off offset:1024
	s_nop 0
	global_load_dwordx4 v[44:47], v[54:55], off
	global_load_dwordx4 v[48:51], v[54:55], off offset:1024
	v_mov_b32_e32 v60, 0x260
	v_lshlrev_b64 v[2:3], 10, v[2:3]
	s_waitcnt vmcnt(10)
	v_pk_add_f32 v[54:55], v[8:9], v[4:5]
	v_pk_add_f32 v[56:57], v[10:11], v[6:7]
	global_load_dwordx4 v[4:7], v0, s[8:9]
	global_load_dwordx4 v[8:11], v0, s[8:9] offset:1024
	s_waitcnt vmcnt(10)
	v_pk_add_f32 v[16:17], v[12:13], v[16:17]
	v_lshl_add_u64 v[12:13], s[4:5], 0, v[52:53]
	v_pk_add_f32 v[18:19], v[14:15], v[18:19]
	v_lshl_add_u64 v[52:53], v[12:13], 0, v[0:1]
	global_load_dwordx4 v[12:15], v0, s[10:11]
	s_mov_b32 s9, 0xf800000
	s_mov_b32 s8, 0x43000000
	s_waitcnt vmcnt(10)
	v_pk_add_f32 v[20:21], v[54:55], v[20:21]
	v_pk_add_f32 v[22:23], v[56:57], v[22:23]
	s_waitcnt vmcnt(9)
	v_pk_add_f32 v[24:25], v[16:17], v[24:25]
	v_pk_add_f32 v[26:27], v[18:19], v[26:27]
	global_load_dwordx4 v[16:19], v0, s[10:11] offset:1024
	s_waitcnt vmcnt(9)
	v_pk_add_f32 v[20:21], v[20:21], v[28:29]
	v_pk_add_f32 v[22:23], v[22:23], v[30:31]
	s_waitcnt vmcnt(8)
	v_pk_add_f32 v[24:25], v[24:25], v[32:33]
	s_waitcnt vmcnt(7)
	v_pk_add_f32 v[20:21], v[20:21], v[36:37]
	v_pk_add_f32 v[22:23], v[22:23], v[38:39]
	s_waitcnt vmcnt(5)
	v_pk_add_f32 v[20:21], v[20:21], v[44:45]
	v_pk_add_f32 v[22:23], v[22:23], v[46:47]
	v_add_f32_e32 v0, 0, v20
	v_add_f32_e32 v0, v0, v21
	v_pk_add_f32 v[24:25], v[24:25], v[40:41]
	v_add_f32_e32 v0, v0, v22
	v_pk_add_f32 v[26:27], v[26:27], v[34:35]
	s_waitcnt vmcnt(4)
	v_pk_add_f32 v[24:25], v[24:25], v[48:49]
	v_add_f32_e32 v0, v0, v23
	v_pk_add_f32 v[26:27], v[26:27], v[42:43]
	v_add_f32_e32 v0, v0, v24
	v_pk_add_f32 v[26:27], v[26:27], v[50:51]
	v_add_f32_e32 v0, v0, v25
	v_add_f32_e32 v0, v0, v26
	v_add_f32_e32 v0, v0, v27
	s_nop 1
	v_add_f32_dpp v0, v0, v0 quad_perm:[1,0,3,2] row_mask:0xf bank_mask:0xf bound_ctrl:1
	s_nop 1
	v_add_f32_dpp v0, v0, v0 quad_perm:[2,3,0,1] row_mask:0xf bank_mask:0xf bound_ctrl:1
	s_nop 1
	v_add_f32_dpp v0, v0, v0 row_half_mirror row_mask:0xf bank_mask:0xf bound_ctrl:1
	s_nop 1
	v_add_f32_dpp v0, v0, v0 row_mirror row_mask:0xf bank_mask:0xf bound_ctrl:1
	s_nop 0
	v_readlane_b32 s4, v0, 16
	v_readlane_b32 s5, v0, 48
	v_readlane_b32 s0, v0, 0
	v_readlane_b32 s1, v0, 32
	v_mov_b32_e32 v28, s4
	v_mov_b32_e32 v29, s5
	v_pk_add_f32 v[28:29], s[0:1], v[28:29]
	s_nop 0
	v_add_f32_e32 v0, v28, v29
	v_mul_f32_e32 v0, 0x3b000000, v0
	v_pk_add_f32 v[20:21], v[20:21], v[0:1] op_sel_hi:[1,0] neg_lo:[0,1] neg_hi:[0,1]
	v_pk_add_f32 v[22:23], v[22:23], v[0:1] op_sel_hi:[1,0] neg_lo:[0,1] neg_hi:[0,1]
	v_pk_mul_f32 v[28:29], v[20:21], v[20:21]
	v_pk_add_f32 v[24:25], v[24:25], v[0:1] op_sel_hi:[1,0] neg_lo:[0,1] neg_hi:[0,1]
	v_pk_add_f32 v[26:27], v[26:27], v[0:1] op_sel_hi:[1,0] neg_lo:[0,1] neg_hi:[0,1]
	v_pk_mul_f32 v[30:31], v[22:23], v[22:23]
	v_add_f32_e32 v0, v28, v29
	v_add_f32_e32 v0, v0, v30
	v_pk_mul_f32 v[32:33], v[24:25], v[24:25]
	v_add_f32_e32 v0, v0, v31
	v_add_f32_e32 v0, v0, v32
	v_pk_mul_f32 v[34:35], v[26:27], v[26:27]
	v_add_f32_e32 v0, v0, v33
	v_add_f32_e32 v0, v0, v34
	v_add_f32_e32 v0, v0, v35
	s_waitcnt vmcnt(3)
	v_pk_mul_f32 v[4:5], v[4:5], v[20:21]
	v_add_f32_dpp v0, v0, v0 quad_perm:[1,0,3,2] row_mask:0xf bank_mask:0xf bound_ctrl:1
	v_pk_mul_f32 v[6:7], v[6:7], v[22:23]
	s_waitcnt vmcnt(2)
	v_pk_mul_f32 v[8:9], v[8:9], v[24:25]
	v_add_f32_dpp v0, v0, v0 quad_perm:[2,3,0,1] row_mask:0xf bank_mask:0xf bound_ctrl:1
	v_pk_mul_f32 v[10:11], v[10:11], v[26:27]
	s_nop 0
	v_add_f32_dpp v0, v0, v0 row_half_mirror row_mask:0xf bank_mask:0xf bound_ctrl:1
	s_nop 1
	v_add_f32_dpp v0, v0, v0 row_mirror row_mask:0xf bank_mask:0xf bound_ctrl:1
	s_nop 0
	v_readlane_b32 s4, v0, 16
	v_readlane_b32 s5, v0, 48
	v_readlane_b32 s0, v0, 0
	v_readlane_b32 s1, v0, 32
	v_mov_b32_e32 v28, s4
	v_mov_b32_e32 v29, s5
	v_pk_add_f32 v[28:29], s[0:1], v[28:29]
	s_nop 0
	v_add_f32_e32 v0, v28, v29
	v_fmac_f32_e32 v59, 0x3b000000, v0
	v_mul_f32_e32 v0, 0x4f800000, v59
	v_cmp_gt_f32_e32 vcc, s9, v59
	s_nop 1
	v_cndmask_b32_e32 v0, v59, v0, vcc
	v_sqrt_f32_e32 v28, v0
	s_nop 0
	v_add_u32_e32 v20, -1, v28
	v_add_u32_e32 v21, 1, v28
	v_fma_f32 v22, -v20, v28, v0
	v_fma_f32 v23, -v21, v28, v0
	v_cmp_ge_f32_e64 s[0:1], 0, v22
	s_nop 1
	v_cndmask_b32_e64 v20, v28, v20, s[0:1]
	v_cmp_lt_f32_e64 s[0:1], 0, v23
	s_nop 1
	v_cndmask_b32_e64 v20, v20, v21, s[0:1]
	v_mul_f32_e32 v21, 0x37800000, v20
	v_cndmask_b32_e32 v20, v20, v21, vcc
	v_cmp_class_f32_e32 vcc, v0, v60
	s_nop 1
	v_cndmask_b32_e32 v0, v20, v0, vcc
	v_div_scale_f32 v20, s[0:1], v0, v0, 1.0
	v_rcp_f32_e32 v21, v20
	v_div_scale_f32 v22, vcc, 1.0, v0, 1.0
	v_fma_f32 v23, -v20, v21, 1.0
	v_fmac_f32_e32 v21, v23, v21
	v_mul_f32_e32 v23, v22, v21
	v_fma_f32 v24, -v20, v23, v22
	v_fmac_f32_e32 v23, v24, v21
	v_fma_f32 v20, -v20, v23, v22
	v_div_fmas_f32 v20, v20, v21, v23
	v_div_fixup_f32 v0, v20, v0, 1.0
	s_waitcnt vmcnt(1)
	v_pk_fma_f32 v[4:5], v[0:1], v[4:5], v[12:13] op_sel_hi:[0,1,1]
	v_pk_fma_f32 v[6:7], v[0:1], v[6:7], v[14:15] op_sel_hi:[0,1,1]
	s_waitcnt vmcnt(0)
	v_pk_fma_f32 v[8:9], v[0:1], v[8:9], v[16:17] op_sel_hi:[0,1,1]
	v_fma_mixlo_f16 v12, v4, s8, 0
	v_pk_fma_f32 v[10:11], v[0:1], v[10:11], v[18:19] op_sel_hi:[0,1,1]
	global_store_dwordx4 v[52:53], v[4:7], off
	global_store_dwordx4 v[52:53], v[8:11], off offset:1024
	v_mul_f32_e32 v0, 0x43000000, v4
	v_fma_mixlo_f16 v4, v4, s8, -v12 op_sel_hi:[0,0,1]
	v_fma_mixlo_f16 v12, v8, s8, 0
	v_mul_f32_e32 v13, 0x43000000, v8
	v_fma_mixlo_f16 v8, v8, s8, -v12 op_sel_hi:[0,0,1]
	v_mul_f32_e32 v12, 0x43000000, v5
	v_fma_mixlo_f16 v14, v5, s8, 0
	v_cvt_pk_f16_f32 v12, v0, v12
	v_mul_f32_e32 v0, 0x43000000, v9
	v_pk_mul_f32 v[16:17], v[6:7], s[8:9] op_sel_hi:[1,0]
	v_fma_mixhi_f16 v4, v5, s8, -v14 op_sel_hi:[0,0,1]
	v_cvt_pk_f16_f32 v14, v13, v0
	v_cvt_pk_f16_f32 v13, v16, v17
	v_pk_mul_f32 v[18:19], v[10:11], s[8:9] op_sel_hi:[1,0]
	v_cvt_f32_f16_e32 v16, v13
	v_cvt_f32_f16_sdwa v17, v13 dst_sel:DWORD dst_unused:UNUSED_PAD src0_sel:WORD_1
	v_cvt_pk_f16_f32 v15, v18, v19
	v_cvt_f32_f16_e32 v18, v15
	v_cvt_f32_f16_sdwa v19, v15 dst_sel:DWORD dst_unused:UNUSED_PAD src0_sel:WORD_1
	v_fma_mixlo_f16 v5, v9, s8, 0
	v_pk_fma_f32 v[6:7], v[6:7], s[8:9], v[16:17] op_sel_hi:[1,0,1] neg_lo:[0,0,1] neg_hi:[0,0,1]
	v_fma_mixhi_f16 v8, v9, s8, -v5 op_sel_hi:[0,0,1]
	v_cvt_pk_f16_f32 v5, v6, v7
	v_pk_fma_f32 v[6:7], v[10:11], s[8:9], v[18:19] op_sel_hi:[1,0,1] neg_lo:[0,0,1] neg_hi:[0,0,1]
	v_lshlrev_b32_e32 v0, 1, v58
	v_cvt_pk_f16_f32 v9, v6, v7
	v_lshl_add_u64 v[6:7], s[6:7], 0, v[2:3]
	v_lshl_add_u64 v[2:3], s[2:3], 0, v[2:3]
	v_lshl_add_u64 v[6:7], v[6:7], 0, v[0:1]
	v_lshl_add_u64 v[0:1], v[2:3], 0, v[0:1]
	global_store_dwordx2 v[6:7], v[12:13], off
	global_store_dwordx2 v[6:7], v[14:15], off offset:512
	global_store_dwordx2 v[0:1], v[4:5], off
	global_store_dwordx2 v[0:1], v[8:9], off offset:512
	s_endpgm
	s_endpgm
	s_endpgm
	s_endpgm
	s_endpgm
	s_endpgm
	s_endpgm
	s_endpgm
	s_endpgm
	s_endpgm
	s_endpgm
	s_endpgm
	s_endpgm
	s_endpgm
	s_endpgm
	s_endpgm

.LBB22_5:
	v_lshlrev_b32_e32 v0, 2, v0
	v_and_b32_e32 v66, 0xfc, v0
	v_lshlrev_b64 v[4:5], 11, v[4:5]
	v_lshlrev_b32_e32 v0, 2, v66
	v_mov_b32_e32 v1, 0
	s_waitcnt lgkmcnt(0)
	v_lshl_add_u64 v[4:5], s[18:19], 0, v[4:5]
	v_lshl_add_u64 v[20:21], v[4:5], 0, v[0:1]
	global_load_dwordx4 v[4:7], v[20:21], off
	global_load_dwordx4 v[8:11], v0, s[16:17]
	global_load_dwordx4 v[12:15], v0, s[16:17] offset:1024
	global_load_dwordx4 v[16:19], v[20:21], off offset:1024
	v_lshlrev_b64 v[48:49], 11, v[2:3]
	v_lshl_add_u64 v[40:41], s[14:15], 0, v[48:49]
	v_lshl_add_u64 v[28:29], v[40:41], 0, v[0:1]
	global_load_dwordx4 v[20:23], v[28:29], off
	global_load_dwordx4 v[24:27], v[28:29], off offset:1024
	s_load_dwordx2 s[0:1], s[0:1], 0x8
	v_lshlrev_b64 v[2:3], 10, v[2:3]
	s_waitcnt lgkmcnt(0)
	v_lshl_add_u64 v[28:29], s[0:1], 2, v[40:41]
	v_lshl_add_u64 v[42:43], v[28:29], 0, v[0:1]
	v_mad_u64_u32 v[36:37], s[12:13], s0, 12, v[40:41]
	v_lshl_add_u64 v[32:33], s[0:1], 3, v[40:41]
	global_load_dwordx4 v[28:31], v[42:43], off
	v_mov_b32_e32 v38, v37
	v_lshl_add_u64 v[44:45], v[32:33], 0, v[0:1]
	v_mad_u64_u32 v[38:39], s[12:13], s1, 12, v[38:39]
	global_load_dwordx4 v[32:35], v[44:45], off
	v_mov_b32_e32 v37, v38
	v_lshl_add_u64 v[46:47], v[36:37], 0, v[0:1]
	global_load_dwordx4 v[36:39], v[46:47], off
	v_mad_u64_u32 v[52:53], s[12:13], s0, 20, v[40:41]
	v_mad_u64_u32 v[54:55], s[12:13], s0, 24, v[40:41]
	v_lshl_add_u64 v[50:51], s[0:1], 4, v[40:41]
	v_mad_u64_u32 v[40:41], s[12:13], s0, 28, v[40:41]
	v_lshl_add_u64 v[50:51], v[50:51], 0, v[0:1]
	s_waitcnt vmcnt(7)
	v_pk_add_f32 v[56:57], v[8:9], v[4:5]
	v_mov_b32_e32 v4, v53
	v_pk_add_f32 v[58:59], v[10:11], v[6:7]
	v_mov_b32_e32 v6, v55
	v_mad_u64_u32 v[10:11], s[12:13], s1, 20, v[4:5]
	s_waitcnt vmcnt(5)
	v_pk_add_f32 v[60:61], v[12:13], v[16:17]
	v_mov_b32_e32 v8, v41
	v_mad_u64_u32 v[12:13], s[12:13], s1, 24, v[6:7]
	v_mov_b32_e32 v53, v10
	v_pk_add_f32 v[62:63], v[14:15], v[18:19]
	v_mad_u64_u32 v[14:15], s[0:1], s1, 28, v[8:9]
	global_load_dwordx4 v[4:7], v[50:51], off
	v_mov_b32_e32 v55, v12
	v_lshl_add_u64 v[52:53], v[52:53], 0, v[0:1]
	v_mov_b32_e32 v41, v14
	v_lshl_add_u64 v[54:55], v[54:55], 0, v[0:1]
	global_load_dwordx4 v[12:15], v[52:53], off
	v_lshl_add_u64 v[64:65], v[40:41], 0, v[0:1]
	global_load_dwordx4 v[16:19], v[54:55], off
	global_load_dwordx4 v[8:11], v[42:43], off offset:1024
	s_waitcnt vmcnt(8)
	v_pk_add_f32 v[40:41], v[56:57], v[20:21]
	v_pk_add_f32 v[42:43], v[58:59], v[22:23]
	global_load_dwordx4 v[20:23], v[64:65], off
	s_waitcnt vmcnt(8)
	v_pk_add_f32 v[56:57], v[60:61], v[24:25]
	v_pk_add_f32 v[58:59], v[62:63], v[26:27]
	s_waitcnt vmcnt(7)
	v_pk_add_f32 v[40:41], v[40:41], v[28:29]
	v_pk_add_f32 v[42:43], v[42:43], v[30:31]
	global_load_dwordx4 v[24:27], v[44:45], off offset:1024
	global_load_dwordx4 v[28:31], v[46:47], off offset:1024
	s_waitcnt vmcnt(8)
	v_pk_add_f32 v[44:45], v[40:41], v[32:33]
	v_pk_add_f32 v[46:47], v[42:43], v[34:35]
	global_load_dwordx4 v[32:35], v[50:51], off offset:1024
	global_load_dwordx4 v[40:43], v[52:53], off offset:1024
	s_waitcnt vmcnt(9)
	v_pk_add_f32 v[50:51], v[44:45], v[36:37]
	v_pk_add_f32 v[52:53], v[46:47], v[38:39]
	global_load_dwordx4 v[36:39], v[54:55], off offset:1024
	global_load_dwordx4 v[44:47], v[64:65], off offset:1024
	s_waitcnt vmcnt(10)
	v_pk_add_f32 v[4:5], v[50:51], v[4:5]
	v_pk_add_f32 v[6:7], v[52:53], v[6:7]
	s_waitcnt vmcnt(9)
	v_pk_add_f32 v[50:51], v[4:5], v[12:13]
	v_pk_add_f32 v[52:53], v[6:7], v[14:15]
	global_load_dwordx4 v[4:7], v0, s[8:9]
	global_load_dwordx4 v[12:15], v0, s[10:11]
	s_waitcnt vmcnt(10)
	v_pk_add_f32 v[16:17], v[50:51], v[16:17]
	v_pk_add_f32 v[18:19], v[52:53], v[18:19]
	s_waitcnt vmcnt(9)
	v_pk_add_f32 v[8:9], v[56:57], v[8:9]
	s_waitcnt vmcnt(8)
	v_pk_add_f32 v[50:51], v[16:17], v[20:21]
	v_pk_add_f32 v[52:53], v[18:19], v[22:23]
	global_load_dwordx4 v[16:19], v0, s[8:9] offset:1024
	global_load_dwordx4 v[20:23], v0, s[10:11] offset:1024
	v_pk_add_f32 v[10:11], v[58:59], v[10:11]
	s_waitcnt vmcnt(9)
	v_pk_add_f32 v[8:9], v[8:9], v[24:25]
	v_add_f32_e32 v24, 0, v50
	s_waitcnt vmcnt(8)
	v_pk_add_f32 v[8:9], v[8:9], v[28:29]
	v_pk_add_f32 v[10:11], v[10:11], v[26:27]
	s_waitcnt vmcnt(7)
	v_pk_add_f32 v[8:9], v[8:9], v[32:33]
	v_add_f32_e32 v24, v24, v51
	s_waitcnt vmcnt(6)
	v_pk_add_f32 v[8:9], v[8:9], v[40:41]
	v_pk_add_f32 v[10:11], v[10:11], v[30:31]
	v_add_f32_e32 v24, v24, v52
	s_waitcnt vmcnt(5)
	v_pk_add_f32 v[8:9], v[8:9], v[36:37]
	v_pk_add_f32 v[10:11], v[10:11], v[34:35]
	v_add_f32_e32 v24, v24, v53
	s_waitcnt vmcnt(4)
	v_pk_add_f32 v[8:9], v[8:9], v[44:45]
	v_pk_add_f32 v[10:11], v[10:11], v[42:43]
	v_add_f32_e32 v24, v24, v8
	v_pk_add_f32 v[10:11], v[10:11], v[38:39]
	v_add_f32_e32 v24, v24, v9
	v_pk_add_f32 v[10:11], v[10:11], v[46:47]
	s_nop 0
	v_add_f32_e32 v24, v24, v10
	v_add_f32_e32 v24, v24, v11
	s_nop 1
	v_add_f32_dpp v24, v24, v24 quad_perm:[1,0,3,2] row_mask:0xf bank_mask:0xf bound_ctrl:1
	s_nop 1
	v_add_f32_dpp v24, v24, v24 quad_perm:[2,3,0,1] row_mask:0xf bank_mask:0xf bound_ctrl:1
	s_nop 1
	v_add_f32_dpp v24, v24, v24 row_half_mirror row_mask:0xf bank_mask:0xf bound_ctrl:1
	s_nop 1
	v_add_f32_dpp v24, v24, v24 row_mirror row_mask:0xf bank_mask:0xf bound_ctrl:1
	s_nop 0
	v_readlane_b32 s8, v24, 16
	v_readlane_b32 s9, v24, 48
	v_readlane_b32 s0, v24, 0
	v_readlane_b32 s1, v24, 32
	v_mov_b32_e32 v24, s8
	v_mov_b32_e32 v25, s9
	v_pk_add_f32 v[24:25], s[0:1], v[24:25]
	s_nop 0
	v_add_f32_e32 v24, v24, v25
	v_mul_f32_e32 v24, 0x3b000000, v24
	v_pk_add_f32 v[26:27], v[50:51], v[24:25] op_sel_hi:[1,0] neg_lo:[0,1] neg_hi:[0,1]
	v_pk_add_f32 v[30:31], v[52:53], v[24:25] op_sel_hi:[1,0] neg_lo:[0,1] neg_hi:[0,1]
	v_pk_mul_f32 v[28:29], v[26:27], v[26:27]
	v_pk_mul_f32 v[32:33], v[30:31], v[30:31]
	v_add_f32_e32 v28, v28, v29
	v_pk_add_f32 v[8:9], v[8:9], v[24:25] op_sel_hi:[1,0] neg_lo:[0,1] neg_hi:[0,1]
	v_add_f32_e32 v28, v28, v32
	v_pk_mul_f32 v[34:35], v[8:9], v[8:9]
	v_add_f32_e32 v28, v28, v33
	v_pk_add_f32 v[10:11], v[10:11], v[24:25] op_sel_hi:[1,0] neg_lo:[0,1] neg_hi:[0,1]
	v_add_f32_e32 v28, v28, v34
	v_pk_mul_f32 v[24:25], v[10:11], v[10:11]
	v_add_f32_e32 v28, v28, v35
	v_add_f32_e32 v24, v28, v24
	v_add_f32_e32 v24, v24, v25
	s_waitcnt vmcnt(3)
	v_pk_mul_f32 v[4:5], v[4:5], v[26:27]
	v_add_f32_dpp v24, v24, v24 quad_perm:[1,0,3,2] row_mask:0xf bank_mask:0xf bound_ctrl:1
	v_pk_mul_f32 v[6:7], v[6:7], v[30:31]
	s_waitcnt vmcnt(1)
	v_pk_mul_f32 v[8:9], v[16:17], v[8:9]
	v_add_f32_dpp v24, v24, v24 quad_perm:[2,3,0,1] row_mask:0xf bank_mask:0xf bound_ctrl:1
	v_pk_mul_f32 v[10:11], v[18:19], v[10:11]
	s_nop 0
	v_add_f32_dpp v24, v24, v24 row_half_mirror row_mask:0xf bank_mask:0xf bound_ctrl:1
	s_nop 1
	v_add_f32_dpp v24, v24, v24 row_mirror row_mask:0xf bank_mask:0xf bound_ctrl:1
	s_nop 0
	v_readlane_b32 s8, v24, 16
	v_readlane_b32 s9, v24, 48
	v_readlane_b32 s0, v24, 0
	v_readlane_b32 s1, v24, 32
	v_mov_b32_e32 v24, s8
	v_mov_b32_e32 v25, s9
	v_pk_add_f32 v[24:25], s[0:1], v[24:25]
	s_mov_b32 s0, 0xf800000
	v_add_f32_e32 v24, v24, v25
	v_mov_b32_e32 v25, 0x3727c5ac
	v_fmac_f32_e32 v25, 0x3b000000, v24
	v_mul_f32_e32 v24, 0x4f800000, v25
	v_cmp_gt_f32_e32 vcc, s0, v25
	s_nop 1
	v_cndmask_b32_e32 v24, v25, v24, vcc
	v_sqrt_f32_e32 v25, v24
	s_nop 0
	v_add_u32_e32 v28, -1, v25
	v_fma_f32 v29, -v28, v25, v24
	v_cmp_ge_f32_e64 s[0:1], 0, v29
	v_add_u32_e32 v29, 1, v25
	s_nop 0
	v_cndmask_b32_e64 v28, v25, v28, s[0:1]
	v_fma_f32 v25, -v29, v25, v24
	v_cmp_lt_f32_e64 s[0:1], 0, v25
	s_nop 1
	v_cndmask_b32_e64 v25, v28, v29, s[0:1]
	v_mul_f32_e32 v28, 0x37800000, v25
	v_cndmask_b32_e32 v25, v25, v28, vcc
	v_mov_b32_e32 v28, 0x260
	v_cmp_class_f32_e32 vcc, v24, v28
	s_nop 1
	v_cndmask_b32_e32 v28, v25, v24, vcc
	v_div_scale_f32 v29, s[0:1], v28, v28, 1.0
	v_rcp_f32_e32 v32, v29
	v_lshl_add_u64 v[24:25], s[4:5], 0, v[48:49]
	v_lshl_add_u64 v[24:25], v[24:25], 0, v[0:1]
	s_mov_b32 s0, 0x43000000
	v_fma_f32 v0, -v29, v32, 1.0
	v_fmac_f32_e32 v32, v0, v32
	v_div_scale_f32 v0, vcc, 1.0, v28, 1.0
	v_mul_f32_e32 v33, v0, v32
	v_fma_f32 v34, -v29, v33, v0
	v_fmac_f32_e32 v33, v34, v32
	v_fma_f32 v0, -v29, v33, v0
	v_div_fmas_f32 v0, v0, v32, v33
	v_div_fixup_f32 v0, v0, v28, 1.0
	v_pk_fma_f32 v[4:5], v[0:1], v[4:5], v[12:13] op_sel_hi:[0,1,1]
	v_pk_fma_f32 v[6:7], v[0:1], v[6:7], v[14:15] op_sel_hi:[0,1,1]
	s_waitcnt vmcnt(0)
	v_pk_fma_f32 v[8:9], v[0:1], v[8:9], v[20:21] op_sel_hi:[0,1,1]
	v_fma_mixlo_f16 v12, v4, s0, 0
	v_pk_fma_f32 v[10:11], v[0:1], v[10:11], v[22:23] op_sel_hi:[0,1,1]
	global_store_dwordx4 v[24:25], v[4:7], off
	global_store_dwordx4 v[24:25], v[8:11], off offset:1024
	v_mul_f32_e32 v0, 0x43000000, v4
	v_fma_mixlo_f16 v4, v4, s0, -v12 op_sel_hi:[0,0,1]
	v_fma_mixlo_f16 v12, v8, s0, 0
	v_mul_f32_e32 v13, 0x43000000, v8
	v_fma_mixlo_f16 v8, v8, s0, -v12 op_sel_hi:[0,0,1]
	v_mul_f32_e32 v12, 0x43000000, v5
	v_fma_mixlo_f16 v14, v5, s0, 0
	v_cvt_pk_f16_f32 v12, v0, v12
	v_mul_f32_e32 v0, 0x43000000, v9
	v_pk_mul_f32 v[16:17], v[6:7], s[0:1] op_sel_hi:[1,0]
	v_fma_mixhi_f16 v4, v5, s0, -v14 op_sel_hi:[0,0,1]
	v_cvt_pk_f16_f32 v14, v13, v0
	v_cvt_pk_f16_f32 v13, v16, v17
	v_pk_mul_f32 v[18:19], v[10:11], s[0:1] op_sel_hi:[1,0]
	v_cvt_f32_f16_e32 v16, v13
	v_cvt_f32_f16_sdwa v17, v13 dst_sel:DWORD dst_unused:UNUSED_PAD src0_sel:WORD_1
	v_cvt_pk_f16_f32 v15, v18, v19
	v_cvt_f32_f16_e32 v18, v15
	v_cvt_f32_f16_sdwa v19, v15 dst_sel:DWORD dst_unused:UNUSED_PAD src0_sel:WORD_1
	v_fma_mixlo_f16 v5, v9, s0, 0
	v_pk_fma_f32 v[6:7], v[6:7], s[0:1], v[16:17] op_sel_hi:[1,0,1] neg_lo:[0,0,1] neg_hi:[0,0,1]
	v_fma_mixhi_f16 v8, v9, s0, -v5 op_sel_hi:[0,0,1]
	v_cvt_pk_f16_f32 v5, v6, v7
	v_pk_fma_f32 v[6:7], v[10:11], s[0:1], v[18:19] op_sel_hi:[1,0,1] neg_lo:[0,0,1] neg_hi:[0,0,1]
	v_lshlrev_b32_e32 v0, 1, v66
	v_cvt_pk_f16_f32 v9, v6, v7
	v_lshl_add_u64 v[6:7], s[6:7], 0, v[2:3]
	v_lshl_add_u64 v[2:3], s[2:3], 0, v[2:3]
	v_lshl_add_u64 v[6:7], v[6:7], 0, v[0:1]
	v_lshl_add_u64 v[0:1], v[2:3], 0, v[0:1]
	global_store_dwordx2 v[6:7], v[12:13], off
	global_store_dwordx2 v[6:7], v[14:15], off offset:512
	global_store_dwordx2 v[0:1], v[4:5], off
	global_store_dwordx2 v[0:1], v[8:9], off offset:512
	s_endpgm
	s_endpgm
	s_endpgm
	s_endpgm
	s_endpgm
	s_endpgm
	s_endpgm
	s_endpgm
	s_endpgm
	s_endpgm
	s_endpgm
	s_endpgm
	s_endpgm
	s_endpgm
	s_endpgm
	s_endpgm
	s_endpgm
	s_endpgm
	s_endpgm
	s_endpgm
	s_endpgm
	s_endpgm
	s_endpgm
	s_endpgm
	s_endpgm
	s_endpgm
	s_endpgm
	s_endpgm
	s_endpgm
	s_endpgm
	s_endpgm
	s_endpgm
	s_endpgm
	s_endpgm
	s_endpgm
	s_endpgm
	s_endpgm
	s_endpgm
	s_endpgm
	s_endpgm
	s_endpgm
	s_endpgm
	s_endpgm
	s_endpgm
	s_endpgm
	s_endpgm
	s_endpgm
	s_endpgm
	s_endpgm
	s_endpgm
	s_endpgm
	s_endpgm
	s_endpgm
	s_endpgm
	s_endpgm
	s_endpgm
	s_endpgm
	s_endpgm
	s_endpgm
	s_endpgm
	s_endpgm
